# speedup vs baseline: 1.0336x; 1.0018x over previous
.LBB2_93:
	ds_read_b128 v[18:21], v125 offset:8192
	ds_read_b128 v[34:37], v125 offset:9216
	v_cvt_pkrtz_f16_f32 v50, v74, v75
	v_cvt_pkrtz_f16_f32 v51, v76, v77
	v_cvt_pkrtz_f16_f32 v52, v82, v83
	v_cvt_pkrtz_f16_f32 v53, v84, v85
	v_cvt_pkrtz_f16_f32 v62, v86, v87
	v_cvt_pkrtz_f16_f32 v63, v88, v89
	v_cvt_pkrtz_f16_f32 v64, v94, v95
	s_waitcnt lgkmcnt(0)
	v_mfma_f32_32x32x16_f16 v[18:33], v[18:21], v[50:53], 0
	v_cvt_pkrtz_f16_f32 v65, v110, v111
	ds_read_b128 v[38:41], v125 offset:10240
	v_cvt_pkrtz_f16_f32 v78, v108, v109
	v_cvt_pkrtz_f16_f32 v79, v106, v107
	v_cvt_pkrtz_f16_f32 v80, v104, v105
	v_cvt_pkrtz_f16_f32 v81, v100, v101
	s_add_i32 s0, 0, 0x1a800
	v_mfma_f32_32x32x16_f16 v[18:33], v[34:37], v[62:65], v[18:33]
	v_lshl_add_u32 v99, v165, 1, s0
	ds_read_b128 v[2:5], v125
	ds_read_b128 v[58:61], v125 offset:1024
	ds_read_b128 v[120:123], v125 offset:2048
	ds_read_b128 v[174:177], v125 offset:3072
	ds_read_b128 v[178:181], v125 offset:4096
	ds_read_b128 v[182:185], v125 offset:5120
	ds_read_b128 v[34:37], v125 offset:11264
	ds_read_b128 v[186:189], v125 offset:6144
	ds_read_b128 v[190:193], v125 offset:7168
	v_cvt_pkrtz_f16_f32 v114, v96, v97
	v_cvt_pkrtz_f16_f32 v115, v92, v93
	s_waitcnt lgkmcnt(0)
	v_mfma_f32_32x32x16_f16 v[18:33], v[38:41], v[78:81], v[18:33]
	ds_read_b128 v[194:197], v99 offset:11648
	ds_read_b128 v[198:201], v99 offset:11936
	ds_read_b128 v[38:41], v125 offset:12288
	v_cvt_pkrtz_f16_f32 v116, v90, v91
	v_cvt_pkrtz_f16_f32 v117, v102, v103
	ds_read_b128 v[202:205], v99 offset:12224
	ds_read_b128 v[206:209], v99 offset:12512
	ds_read_b128 v[210:213], v99 offset:12800
	ds_read_b128 v[54:57], v99 offset:13088
	ds_read_b128 v[70:73], v99 offset:13376
	ds_read_b128 v[66:69], v99 offset:13664
	ds_read_b128 v[214:217], v125 offset:13312
	ds_read_b128 v[218:221], v99 offset:13952
	ds_read_b128 v[222:225], v125 offset:14336
	ds_read_b128 v[226:229], v125 offset:15360
	ds_read_b128 v[230:233], v99 offset:14240
	s_mov_b32 s16, 0xff61b1e6
	s_mov_b32 s17, 0
	v_mfma_f32_32x32x16_f16 v[18:33], v[34:37], v[114:117], v[18:33]
	s_waitcnt lgkmcnt(0)
	v_mfma_f32_32x32x16_f16 v[34:49], v[38:41], v[50:53], 0
	s_nop 9
	v_add_f32_e32 v112, v18, v218
	v_add_f32_e32 v113, v19, v219
	v_add_f32_e32 v159, v20, v220
	v_add_f32_e32 v161, v21, v221
	ds_read_b128 v[18:21], v99 offset:14528
	v_add_f32_e32 v164, v22, v230
	v_add_f32_e32 v165, v23, v231
	v_mfma_f32_32x32x16_f16 v[34:49], v[214:217], v[62:65], v[34:49]
	v_add_f32_e32 v170, v24, v232
	v_add_f32_e32 v173, v25, v233
	ds_read_b128 v[22:25], v99 offset:14816
	s_waitcnt lgkmcnt(0)
	v_add_f32_e32 v26, v26, v18
	v_add_f32_e32 v27, v27, v19
	v_add_f32_e32 v28, v28, v20
	v_add_f32_e32 v29, v29, v21
	v_mfma_f32_32x32x16_f16 v[34:49], v[222:225], v[78:81], v[34:49]
	ds_read_b128 v[18:21], v99 offset:15104
	v_add_f32_e32 v30, v30, v22
	v_add_f32_e32 v31, v31, v23
	v_add_f32_e32 v32, v32, v24
	v_add_f32_e32 v33, v33, v25
	ds_read_b128 v[22:25], v99 offset:15392
	v_mfma_f32_32x32x16_f16 v[34:49], v[226:229], v[114:117], v[34:49]
	v_mfma_f32_32x32x16_f16 v[2:17], v[2:5], v[50:53], 0
	s_waitcnt lgkmcnt(0)
	s_nop 9
	v_add_f32_e32 v34, v34, v18
	v_add_f32_e32 v35, v35, v19
	v_add_f32_e32 v36, v36, v20
	v_add_f32_e32 v37, v37, v21
	ds_read_b128 v[18:21], v99 offset:15680
	v_add_f32_e32 v38, v38, v22
	v_add_f32_e32 v39, v39, v23
	v_add_f32_e32 v40, v40, v24
	v_add_f32_e32 v41, v41, v25
	ds_read_b128 v[22:25], v99 offset:15968
	s_waitcnt lgkmcnt(0)
	v_add_f32_e32 v42, v42, v18
	v_add_f32_e32 v43, v43, v19
	v_add_f32_e32 v44, v44, v20
	v_add_f32_e32 v45, v45, v21
	v_cvt_pkrtz_f16_f32 v18, v112, v113
	v_cvt_pkrtz_f16_f32 v19, v159, v161
	v_cvt_pkrtz_f16_f32 v20, v164, v165
	v_cvt_pkrtz_f16_f32 v21, v170, v173
	ds_write_b128 v166, v[18:21]
	v_cvt_pkrtz_f16_f32 v18, v26, v27
	v_cvt_pkrtz_f16_f32 v19, v28, v29
	v_cvt_pkrtz_f16_f32 v20, v30, v31
	v_cvt_pkrtz_f16_f32 v21, v32, v33
	v_add_f32_e32 v22, v46, v22
	v_add_f32_e32 v23, v47, v23
	v_add_f32_e32 v24, v48, v24
	v_add_f32_e32 v25, v49, v25
	ds_write_b128 v166, v[18:21] offset:32
	v_cvt_pkrtz_f16_f32 v18, v34, v35
	v_cvt_pkrtz_f16_f32 v19, v36, v37
	v_cvt_pkrtz_f16_f32 v20, v38, v39
	v_cvt_pkrtz_f16_f32 v21, v40, v41
	ds_write_b128 v166, v[18:21] offset:64
	v_cvt_pkrtz_f16_f32 v18, v42, v43
	v_cvt_pkrtz_f16_f32 v19, v44, v45
	v_cvt_pkrtz_f16_f32 v20, v22, v23
	v_cvt_pkrtz_f16_f32 v21, v24, v25
	ds_write_b128 v166, v[18:21] offset:96
	ds_read_b128 v[18:21], v125 offset:16384
	ds_read_b128 v[22:25], v125 offset:17408
	s_waitcnt lgkmcnt(0)
	v_mfma_f32_32x32x16_f16 v[30:45], v[50:53], v[18:21], 0
	v_add_u32_e32 v112, v167, v162
	v_add_u32_e32 v159, v171, v172
	v_mfma_f32_32x32x16_f16 v[2:17], v[58:61], v[62:65], v[2:17]
	v_mfma_f32_32x32x16_f16 v[30:45], v[62:65], v[22:25], v[30:45]
	ds_read_b128 v[18:21], v125 offset:18432
	ds_read_b128 v[22:25], v125 offset:19456
	v_mfma_f32_32x32x16_f16 v[2:17], v[120:123], v[78:81], v[2:17]
	s_waitcnt lgkmcnt(0)
	v_mfma_f32_32x32x16_f16 v[30:45], v[78:81], v[18:21], v[30:45]
	v_add3_u32 v18, s0, v168, v160
	ds_read_b32 v46, v18 offset:16256
	v_mfma_f32_32x32x16_f16 v[2:17], v[174:177], v[114:117], v[2:17]
	v_mfma_f32_32x32x16_f16 v[30:45], v[114:117], v[22:25], v[30:45]
	s_nop 10
	v_fmamk_f32 v58, v194, 0x3e38aa3b, v2
	v_fmamk_f32 v59, v195, 0x3e38aa3b, v3
	v_fmamk_f32 v99, v198, 0x3e38aa3b, v6
	v_fmamk_f32 v113, v202, 0x3e38aa3b, v10
	v_fmamk_f32 v120, v203, 0x3e38aa3b, v11
	v_fmamk_f32 v121, v204, 0x3e38aa3b, v12
	v_fmamk_f32 v122, v205, 0x3e38aa3b, v13
	s_waitcnt lgkmcnt(0)
	v_add_f32_e32 v2, v46, v30
	v_add_f32_e32 v3, v46, v31
	v_add_f32_e32 v47, v46, v32
	v_add_f32_e32 v48, v46, v33
	v_add_f32_e32 v49, v46, v34
	v_add_f32_e32 v60, v46, v35
	v_add_f32_e32 v61, v46, v36
	v_add_f32_e32 v37, v46, v37
	v_add_f32_e32 v38, v46, v38
	v_add_f32_e32 v39, v46, v39
	v_add_f32_e32 v40, v46, v40
	v_add_f32_e32 v41, v46, v41
	v_add_f32_e32 v42, v46, v42
	v_add_f32_e32 v43, v46, v43
	v_add_f32_e32 v44, v46, v44
	v_add_f32_e32 v45, v46, v45
	v_cvt_pkrtz_f16_f32 v34, v2, v3
	v_cvt_pkrtz_f16_f32 v35, v47, v48
	v_cvt_pkrtz_f16_f32 v36, v49, v60
	v_cvt_pkrtz_f16_f32 v37, v61, v37
	ds_write_b128 v112, v[34:37]
	v_cvt_pkrtz_f16_f32 v34, v38, v39
	v_cvt_pkrtz_f16_f32 v35, v40, v41
	v_cvt_pkrtz_f16_f32 v36, v42, v43
	v_cvt_pkrtz_f16_f32 v37, v44, v45
	ds_write_b128 v112, v[34:37] offset:32
	ds_read_b128 v[34:37], v125 offset:20480
	v_fmamk_f32 v60, v196, 0x3e38aa3b, v4
	v_fmamk_f32 v61, v197, 0x3e38aa3b, v5
	ds_read_b128 v[2:5], v125 offset:21504
	s_waitcnt lgkmcnt(0)
	v_mfma_f32_32x32x16_f16 v[34:49], v[50:53], v[34:37], 0
	v_fmamk_f32 v14, v206, 0x3e38aa3b, v14
	v_fmamk_f32 v15, v207, 0x3e38aa3b, v15
	v_fmamk_f32 v16, v208, 0x3e38aa3b, v16
	v_fmac_f32_e32 v17, 0x3e38aa3b, v209
	v_mfma_f32_32x32x16_f16 v[34:49], v[62:65], v[2:5], v[34:49]
	ds_read_b128 v[2:5], v125 offset:22528
	v_mfma_f32_32x32x16_f16 v[18:33], v[178:181], v[50:53], 0
	v_fmamk_f32 v50, v199, 0x3e38aa3b, v7
	v_fmamk_f32 v51, v200, 0x3e38aa3b, v8
	v_fmamk_f32 v52, v201, 0x3e38aa3b, v9
	ds_read_b128 v[6:9], v125 offset:23552
	s_waitcnt lgkmcnt(0)
	v_mfma_f32_32x32x16_f16 v[34:49], v[78:81], v[2:5], v[34:49]
	v_add3_u32 v2, s0, v169, v160
	ds_read_b32 v2, v2 offset:16256
	s_lshl_b32 s0, s28, 9
	s_add_i32 s0, s0, 0
	s_add_i32 s14, s0, 0x27800
	v_mfma_f32_32x32x16_f16 v[18:33], v[182:185], v[62:65], v[18:33]
	v_mfma_f32_32x32x16_f16 v[34:49], v[114:117], v[6:9], v[34:49]
	v_mfma_f32_32x32x16_f16 v[18:33], v[186:189], v[78:81], v[18:33]
	s_waitcnt lgkmcnt(0)
	s_nop 9
	v_add_f32_e32 v3, v2, v34
	v_add_f32_e32 v4, v2, v35
	v_add_f32_e32 v5, v2, v36
	v_add_f32_e32 v6, v2, v37
	v_add_f32_e32 v7, v2, v38
	v_add_f32_e32 v8, v2, v39
	v_add_f32_e32 v9, v2, v40
	v_add_f32_e32 v10, v2, v41
	v_add_f32_e32 v11, v2, v42
	v_add_f32_e32 v12, v2, v43
	v_add_f32_e32 v13, v2, v44
	v_add_f32_e32 v34, v2, v45
	v_add_f32_e32 v35, v2, v46
	v_add_f32_e32 v36, v2, v47
	v_add_f32_e32 v37, v2, v48
	v_add_f32_e32 v38, v2, v49
	v_cvt_pkrtz_f16_f32 v2, v3, v4
	v_cvt_pkrtz_f16_f32 v3, v5, v6
	v_cvt_pkrtz_f16_f32 v4, v7, v8
	v_cvt_pkrtz_f16_f32 v5, v9, v10
	ds_write_b128 v112, v[2:5] offset:8704
	v_cvt_pkrtz_f16_f32 v2, v11, v12
	v_cvt_pkrtz_f16_f32 v3, v13, v34
	v_cvt_pkrtz_f16_f32 v4, v35, v36
	v_cvt_pkrtz_f16_f32 v5, v37, v38
	ds_write_b128 v112, v[2:5] offset:8736
	s_nop 0
	s_waitcnt lgkmcnt(0)
	s_barrier
	ds_read_b128 v[2:5], v159
	ds_read_b128 v[10:13], v159 offset:32
	v_mfma_f32_32x32x16_f16 v[18:33], v[190:193], v[114:117], v[18:33]
	v_cvt_pkrtz_f16_f32 v6, v58, v59
	v_cvt_pkrtz_f16_f32 v7, v60, v61
	v_cvt_pkrtz_f16_f32 v8, v99, v50
	v_cvt_pkrtz_f16_f32 v9, v51, v52
	v_cvt_pkrtz_f16_f32 v78, v113, v120
	v_cvt_pkrtz_f16_f32 v79, v121, v122
	v_cvt_pkrtz_f16_f32 v80, v14, v15
	s_nop 4
	v_fmamk_f32 v22, v54, 0x3e38aa3b, v22
	v_fmamk_f32 v23, v55, 0x3e38aa3b, v23
	v_fmamk_f32 v24, v56, 0x3e38aa3b, v24
	v_fmamk_f32 v25, v57, 0x3e38aa3b, v25
	s_waitcnt lgkmcnt(1)
	v_mfma_f32_32x32x16_f16 v[50:65], v[2:5], v[6:9], 0
	v_cvt_pkrtz_f16_f32 v81, v16, v17
	ds_read_b128 v[2:5], v159 offset:64
	v_fmamk_f32 v18, v210, 0x3e38aa3b, v18
	v_fmamk_f32 v19, v211, 0x3e38aa3b, v19
	v_fmamk_f32 v20, v212, 0x3e38aa3b, v20
	v_fmamk_f32 v21, v213, 0x3e38aa3b, v21
	v_fmamk_f32 v26, v70, 0x3e38aa3b, v26
	s_waitcnt lgkmcnt(1)
	v_mfma_f32_32x32x16_f16 v[50:65], v[10:13], v[78:81], v[50:65]
	v_fmamk_f32 v27, v71, 0x3e38aa3b, v27
	v_fmamk_f32 v28, v72, 0x3e38aa3b, v28
	v_fmamk_f32 v14, v73, 0x3e38aa3b, v29
	v_cvt_pkrtz_f16_f32 v70, v18, v19
	v_cvt_pkrtz_f16_f32 v71, v20, v21
	v_cvt_pkrtz_f16_f32 v72, v22, v23
	v_cvt_pkrtz_f16_f32 v73, v24, v25
	ds_read_b128 v[10:13], v159 offset:96
	v_fmamk_f32 v15, v66, 0x3e38aa3b, v30
	s_waitcnt lgkmcnt(1)
	v_mfma_f32_32x32x16_f16 v[50:65], v[2:5], v[70:73], v[50:65]
	v_fmamk_f32 v2, v67, 0x3e38aa3b, v31
	v_fmamk_f32 v3, v68, 0x3e38aa3b, v32
	v_fmac_f32_e32 v33, 0x3e38aa3b, v69
	v_cvt_pkrtz_f16_f32 v66, v26, v27
	v_cvt_pkrtz_f16_f32 v67, v28, v14
	v_cvt_pkrtz_f16_f32 v68, v15, v2
	v_cvt_pkrtz_f16_f32 v69, v3, v33
	v_add_u32_e32 v113, v163, v162
	s_waitcnt lgkmcnt(0)
	v_mfma_f32_32x32x16_f16 v[50:65], v[10:13], v[66:69], v[50:65]
	ds_read_b128 v[2:5], v159 offset:4608
	ds_read_b128 v[10:13], v159 offset:4640
	s_waitcnt lgkmcnt(1)
	v_mfma_f32_32x32x16_f16 v[34:49], v[2:5], v[6:9], 0
	s_waitcnt lgkmcnt(0)
	v_mfma_f32_32x32x16_f16 v[34:49], v[10:13], v[78:81], v[34:49]
	ds_read_b128 v[2:5], v159 offset:4672
	ds_read_b128 v[10:13], v159 offset:4704
	s_waitcnt lgkmcnt(1)
	v_mfma_f32_32x32x16_f16 v[34:49], v[2:5], v[70:73], v[34:49]
	s_waitcnt lgkmcnt(0)
	v_mfma_f32_32x32x16_f16 v[34:49], v[10:13], v[66:69], v[34:49]
	ds_read_b128 v[2:5], v159 offset:9216
	ds_read_b128 v[10:13], v159 offset:9248
	s_waitcnt lgkmcnt(1)
	v_mfma_f32_32x32x16_f16 v[18:33], v[2:5], v[6:9], 0
	s_waitcnt lgkmcnt(0)
	v_mfma_f32_32x32x16_f16 v[18:33], v[10:13], v[78:81], v[18:33]
	ds_read_b128 v[2:5], v159 offset:9280
	ds_read_b128 v[10:13], v159 offset:9312
	s_waitcnt lgkmcnt(1)
	v_mfma_f32_32x32x16_f16 v[18:33], v[2:5], v[70:73], v[18:33]
	ds_read_b128 v[2:5], v159 offset:13824
	ds_read_b128 v[114:117], v159 offset:13856
	ds_read_b128 v[120:123], v159 offset:13888
	ds_read_b128 v[164:167], v159 offset:13920
	s_waitcnt lgkmcnt(4)
	v_mfma_f32_32x32x16_f16 v[18:33], v[10:13], v[66:69], v[18:33]
	s_waitcnt lgkmcnt(3)
	v_mfma_f32_32x32x16_f16 v[2:17], v[2:5], v[6:9], 0
	s_waitcnt lgkmcnt(2)
	v_mfma_f32_32x32x16_f16 v[2:17], v[114:117], v[78:81], v[2:17]
	s_waitcnt lgkmcnt(1)
	v_mfma_f32_32x32x16_f16 v[2:17], v[120:123], v[70:73], v[2:17]
	s_waitcnt lgkmcnt(0)
	v_mfma_f32_32x32x16_f16 v[2:17], v[164:167], v[66:69], v[2:17]
	v_mov_b32_e32 v99, 0
	s_nop 10
	s_nop 1
	v_exp_f32_e32 v34, v34
	v_exp_f32_e32 v35, v35
	v_exp_f32_e32 v36, v36
	v_exp_f32_e32 v37, v37
	v_cvt_pkrtz_f16_f32 v34, v34, v35
	v_cvt_pkrtz_f16_f32 v35, v36, v37
	v_exp_f32_e32 v36, v38
	v_exp_f32_e32 v37, v39
	v_exp_f32_e32 v38, v40
	v_exp_f32_e32 v39, v41
	v_exp_f32_e32 v40, v42
	v_exp_f32_e32 v41, v43
	v_exp_f32_e32 v42, v44
	v_exp_f32_e32 v43, v45
	v_cvt_pkrtz_f16_f32 v36, v36, v37
	v_cvt_pkrtz_f16_f32 v37, v38, v39
	v_cvt_pkrtz_f16_f32 v38, v40, v41
	v_cvt_pkrtz_f16_f32 v39, v42, v43
	v_exp_f32_e32 v40, v46
	v_exp_f32_e32 v41, v47
	v_exp_f32_e32 v42, v48
	v_exp_f32_e32 v43, v49
	v_exp_f32_e32 v18, v18
	v_exp_f32_e32 v19, v19
	v_exp_f32_e32 v20, v20
	v_exp_f32_e32 v21, v21
	v_exp_f32_e32 v50, v50
	v_exp_f32_e32 v51, v51
	v_exp_f32_e32 v52, v52
	v_exp_f32_e32 v53, v53
	v_cvt_pkrtz_f16_f32 v40, v40, v41
	v_cvt_pkrtz_f16_f32 v41, v42, v43
	v_cvt_pkrtz_f16_f32 v42, v18, v19
	v_cvt_pkrtz_f16_f32 v43, v20, v21
	v_exp_f32_e32 v18, v22
	v_exp_f32_e32 v19, v23
	v_exp_f32_e32 v20, v24
	v_exp_f32_e32 v21, v25
	v_cvt_pkrtz_f16_f32 v50, v50, v51
	v_cvt_pkrtz_f16_f32 v51, v52, v53
	v_exp_f32_e32 v52, v54
	v_exp_f32_e32 v53, v55
	v_exp_f32_e32 v54, v56
	v_exp_f32_e32 v55, v57
	v_exp_f32_e32 v56, v58
	v_exp_f32_e32 v57, v59
	v_exp_f32_e32 v58, v60
	v_exp_f32_e32 v59, v61
	v_cvt_pkrtz_f16_f32 v44, v18, v19
	v_cvt_pkrtz_f16_f32 v45, v20, v21
	ds_read_b128 v[18:21], v113
	v_exp_f32_e32 v22, v26
	v_exp_f32_e32 v23, v27
	v_cvt_pkrtz_f16_f32 v52, v52, v53
	v_cvt_pkrtz_f16_f32 v53, v54, v55
	v_cvt_pkrtz_f16_f32 v54, v56, v57
	v_cvt_pkrtz_f16_f32 v55, v58, v59
	v_exp_f32_e32 v56, v62
	v_exp_f32_e32 v57, v63
	v_exp_f32_e32 v58, v64
	v_exp_f32_e32 v59, v65
	v_exp_f32_e32 v24, v28
	v_exp_f32_e32 v25, v29
	v_cvt_pkrtz_f16_f32 v46, v22, v23
	v_exp_f32_e32 v48, v30
	v_exp_f32_e32 v49, v31
	v_cvt_pkrtz_f16_f32 v56, v56, v57
	v_cvt_pkrtz_f16_f32 v57, v58, v59
	v_exp_f32_e32 v62, v32
	ds_read_b128 v[58:61], v113 offset:32
	v_cvt_pkrtz_f16_f32 v47, v24, v25
	v_exp_f32_e32 v63, v33
	s_waitcnt lgkmcnt(1)
	v_mfma_f32_32x32x16_f16 v[18:33], v[18:21], v[50:53], 0
	v_cvt_pkrtz_f16_f32 v48, v48, v49
	v_cvt_pkrtz_f16_f32 v49, v62, v63
	ds_read_b128 v[62:65], v113 offset:64
	v_exp_f32_e32 v67, v2
	v_exp_f32_e32 v68, v3
	s_waitcnt lgkmcnt(1)
	v_mfma_f32_32x32x16_f16 v[18:33], v[58:61], v[54:57], v[18:33]
	v_exp_f32_e32 v59, v4
	v_exp_f32_e32 v60, v5
	v_exp_f32_e32 v61, v6
	ds_read_b128 v[2:5], v113 offset:96
	s_waitcnt lgkmcnt(1)
	v_mfma_f32_32x32x16_f16 v[18:33], v[62:65], v[34:37], v[18:33]
	v_exp_f32_e32 v62, v7
	v_exp_f32_e32 v63, v8
	v_exp_f32_e32 v64, v9
	ds_read_b128 v[6:9], v113 offset:128
	s_waitcnt lgkmcnt(1)
	v_mfma_f32_32x32x16_f16 v[18:33], v[2:5], v[38:41], v[18:33]
	v_exp_f32_e32 v10, v10
	ds_read_b128 v[2:5], v113 offset:160
	v_cvt_pkrtz_f16_f32 v58, v67, v68
	v_cvt_pkrtz_f16_f32 v59, v59, v60
	v_cvt_pkrtz_f16_f32 v60, v61, v62
	v_cvt_pkrtz_f16_f32 v61, v63, v64
	s_waitcnt lgkmcnt(1)
	v_mfma_f32_32x32x16_f16 v[18:33], v[6:9], v[42:45], v[18:33]
	v_exp_f32_e32 v11, v11
	v_exp_f32_e32 v12, v12
	v_exp_f32_e32 v13, v13
	ds_read_b128 v[6:9], v113 offset:192
	s_waitcnt lgkmcnt(1)
	v_mfma_f32_32x32x16_f16 v[18:33], v[2:5], v[46:49], v[18:33]
	v_exp_f32_e32 v14, v14
	v_exp_f32_e32 v15, v15
	v_exp_f32_e32 v16, v16
	ds_read_b128 v[2:5], v113 offset:224
	s_waitcnt lgkmcnt(1)
	v_mfma_f32_32x32x16_f16 v[18:33], v[6:9], v[58:61], v[18:33]
	v_exp_f32_e32 v6, v17
	v_cvt_pkrtz_f16_f32 v62, v10, v11
	v_cvt_pkrtz_f16_f32 v63, v12, v13
	v_cvt_pkrtz_f16_f32 v64, v14, v15
	v_cvt_pkrtz_f16_f32 v65, v16, v6
	ds_read_b128 v[6:9], v113 offset:8704
	ds_read_b128 v[66:69], v113 offset:8736
	s_waitcnt lgkmcnt(2)
	v_mfma_f32_32x32x16_f16 v[18:33], v[2:5], v[62:65], v[18:33]
	v_mov_b32_e32 v70, 0
	v_dot2c_f32_f16_e32 v70, 0x3c003c00, v50
	v_dot2c_f32_f16_e32 v70, 0x3c003c00, v51
	v_dot2c_f32_f16_e32 v70, 0x3c003c00, v52
	v_dot2c_f32_f16_e32 v70, 0x3c003c00, v53
	v_dot2c_f32_f16_e32 v70, 0x3c003c00, v54
	v_dot2c_f32_f16_e32 v70, 0x3c003c00, v55
	s_waitcnt lgkmcnt(1)
	v_mfma_f32_32x32x16_f16 v[2:17], v[6:9], v[50:53], 0
	ds_read_b128 v[50:53], v113 offset:8768
	v_dot2c_f32_f16_e32 v70, 0x3c003c00, v56
	v_dot2c_f32_f16_e32 v70, 0x3c003c00, v57
	v_dot2c_f32_f16_e32 v70, 0x3c003c00, v34
	v_dot2c_f32_f16_e32 v70, 0x3c003c00, v35
	v_dot2c_f32_f16_e32 v70, 0x3c003c00, v36
	v_dot2c_f32_f16_e32 v70, 0x3c003c00, v37
	s_waitcnt lgkmcnt(1)
	v_mfma_f32_32x32x16_f16 v[2:17], v[66:69], v[54:57], v[2:17]
	ds_read_b128 v[54:57], v113 offset:8800
	v_dot2c_f32_f16_e32 v70, 0x3c003c00, v38
	v_dot2c_f32_f16_e32 v70, 0x3c003c00, v39
	v_dot2c_f32_f16_e32 v70, 0x3c003c00, v40
	v_dot2c_f32_f16_e32 v70, 0x3c003c00, v41
	v_dot2c_f32_f16_e32 v70, 0x3c003c00, v42
	v_dot2c_f32_f16_e32 v70, 0x3c003c00, v43
	s_waitcnt lgkmcnt(1)
	v_mfma_f32_32x32x16_f16 v[2:17], v[50:53], v[34:37], v[2:17]
	v_dot2c_f32_f16_e32 v70, 0x3c003c00, v44
	ds_read_b128 v[34:37], v113 offset:8832
	v_dot2c_f32_f16_e32 v70, 0x3c003c00, v45
	v_dot2c_f32_f16_e32 v70, 0x3c003c00, v46
	v_dot2c_f32_f16_e32 v70, 0x3c003c00, v47
	v_dot2c_f32_f16_e32 v70, 0x3c003c00, v48
	v_dot2c_f32_f16_e32 v70, 0x3c003c00, v49
	s_waitcnt lgkmcnt(1)
	v_mfma_f32_32x32x16_f16 v[2:17], v[54:57], v[38:41], v[2:17]
	v_dot2c_f32_f16_e32 v70, 0x3c003c00, v58
	v_dot2c_f32_f16_e32 v70, 0x3c003c00, v59
	v_dot2c_f32_f16_e32 v70, 0x3c003c00, v60
	ds_read_b128 v[38:41], v113 offset:8864
	v_dot2c_f32_f16_e32 v70, 0x3c003c00, v61
	v_dot2c_f32_f16_e32 v70, 0x3c003c00, v62
	v_dot2c_f32_f16_e32 v70, 0x3c003c00, v63
	s_waitcnt lgkmcnt(1)
	v_mfma_f32_32x32x16_f16 v[2:17], v[34:37], v[42:45], v[2:17]
	v_dot2c_f32_f16_e32 v70, 0x3c003c00, v64
	v_dot2c_f32_f16_e32 v70, 0x3c003c00, v65
	s_nop 2
	v_mov_b32_e32 v34, v70
	v_mov_b32_e32 v35, v70
	s_nop 1
	v_permlane32_swap_b32_e32 v34, v35
	v_cndmask_b32_e64 v42, v34, v35, s[2:3]
	ds_read_b128 v[34:37], v113 offset:8896
	s_waitcnt lgkmcnt(1)
	v_mfma_f32_32x32x16_f16 v[2:17], v[38:41], v[46:49], v[2:17]
	v_add_f32_e32 v38, v70, v42
	v_rcp_f32_e32 v42, v38
	ds_read_b128 v[38:41], v113 offset:8928
	v_fma_f32 v78, v42, v18, v74
	v_fma_f32 v79, v42, v19, v75
	v_fma_f32 v80, v42, v20, v76
	v_fma_f32 v81, v42, v21, v77
	s_waitcnt lgkmcnt(1)
	v_mfma_f32_32x32x16_f16 v[2:17], v[34:37], v[58:61], v[2:17]
	v_fma_f32 v82, v42, v22, v82
	v_fma_f32 v83, v42, v23, v83
	v_fma_f32 v84, v42, v24, v84
	v_fma_f32 v85, v42, v25, v85
	v_fma_f32 v86, v42, v26, v86
	v_fma_f32 v87, v42, v27, v87
	v_fma_f32 v88, v42, v28, v88
	v_fma_f32 v89, v42, v29, v89
	v_fma_f32 v72, v42, v30, v94
	v_fma_f32 v73, v42, v31, v95
	v_fma_f32 v74, v42, v32, v110
	v_fma_f32 v75, v42, v33, v111
	s_waitcnt lgkmcnt(0)
	v_mfma_f32_32x32x16_f16 v[2:17], v[38:41], v[62:65], v[2:17]
	s_nop 11
	v_fma_f32 v76, v42, v2, v108
	v_fma_f32 v77, v42, v3, v109
	v_fma_f32 v68, v42, v4, v106
	v_fma_f32 v69, v42, v5, v107
	v_fma_f32 v70, v42, v6, v104
	v_fma_f32 v71, v42, v7, v105
	v_pk_fma_f32 v[58:59], v[42:43], v[8:9], v[100:101] op_sel_hi:[0,1,1]
	v_pk_fma_f32 v[66:67], v[42:43], v[10:11], v[96:97] op_sel_hi:[0,1,1]
	v_pk_fma_f32 v[60:61], v[42:43], v[12:13], v[92:93] op_sel_hi:[0,1,1]
	v_pk_fma_f32 v[62:63], v[42:43], v[14:15], v[90:91] op_sel_hi:[0,1,1]
	v_pk_fma_f32 v[64:65], v[42:43], v[16:17], v[102:103] op_sel_hi:[0,1,1]
	v_lshl_add_u64 v[2:3], v[118:119], 1, s[4:5]
	v_lshl_add_u64 v[2:3], v[2:3], 0, v[98:99]
	v_cvt_pk_f16_f32 v5, v80, v81
	v_cvt_pk_f16_f32 v4, v78, v79
	s_waitcnt vmcnt(0)
	s_barrier
	global_store_dwordx2 v[2:3], v[4:5], off
	v_cvt_pk_f16_f32 v5, v84, v85
	v_cvt_pk_f16_f32 v4, v82, v83
	global_store_dwordx2 v[2:3], v[4:5], off offset:16
	v_cvt_pk_f16_f32 v5, v88, v89
	v_cvt_pk_f16_f32 v4, v86, v87
	global_store_dwordx2 v[2:3], v[4:5], off offset:32
	v_cvt_pk_f16_f32 v5, v74, v75
	v_cvt_pk_f16_f32 v4, v72, v73
	global_store_dwordx2 v[2:3], v[4:5], off offset:48
	v_cvt_pk_f16_f32 v5, v68, v69
	v_cvt_pk_f16_f32 v4, v76, v77
	global_store_dwordx2 v[2:3], v[4:5], off offset:64
	v_cvt_pk_f16_f32 v5, v58, v59
	v_cvt_pk_f16_f32 v4, v70, v71
	global_store_dwordx2 v[2:3], v[4:5], off offset:80
	v_cvt_pk_f16_f32 v5, v60, v61
	v_cvt_pk_f16_f32 v4, v66, v67
	global_store_dwordx2 v[2:3], v[4:5], off offset:96
	v_cvt_pk_f16_f32 v5, v64, v65
	v_cvt_pk_f16_f32 v4, v62, v63
	v_cmp_gt_u32_e64 s[0:1], 32, v124
	v_lshl_add_u32 v91, v126, 2, s14
	v_lshl_add_u32 v93, v1, 2, s14
	s_mov_b64 s[4:5], -1
	v_mov_b32_e32 v95, v78
	v_mov_b32_e32 v94, v79
	v_mov_b32_e32 v97, v80
	v_mov_b32_e32 v96, v81
	v_mov_b32_e32 v99, v82
	v_mov_b32_e32 v98, v83
	v_mov_b32_e32 v35, v84
	v_mov_b32_e32 v34, v85
	v_mov_b32_e32 v37, v86
	v_mov_b32_e32 v36, v87
	v_mov_b32_e32 v39, v88
	v_mov_b32_e32 v38, v89
	v_mov_b32_e32 v41, v72
	v_mov_b32_e32 v40, v73
	v_mov_b32_e32 v19, v74
	v_mov_b32_e32 v18, v75
	v_mov_b32_e32 v21, v76
	v_mov_b32_e32 v20, v77
	v_mov_b32_e32 v23, v68
	v_mov_b32_e32 v22, v69
	v_mov_b32_e32 v42, v70
	v_mov_b32_e32 v24, v71
	v_mov_b32_e32 v43, v58
	v_mov_b32_e32 v27, v59
	v_mov_b32_e32 v26, v66
	v_mov_b32_e32 v25, v67
	v_mov_b32_e32 v29, v60
	v_mov_b32_e32 v28, v61
	v_mov_b32_e32 v32, v62
	v_mov_b32_e32 v30, v63
	v_mov_b32_e32 v33, v64
	v_mov_b32_e32 v31, v65
	global_store_dwordx2 v[2:3], v[4:5], off offset:112
	s_branch .LBB2_95
.LBB2_94:
	s_or_b64 exec, exec, s[14:15]
	s_waitcnt lgkmcnt(0)
	s_barrier
	ds_read_b128 v[6:9], v91
	v_cndmask_b32_e64 v3, v4, v5, s[2:3]
	v_add_f32_e32 v10, v2, v3
	ds_read_b128 v[2:5], v91 offset:32
	v_mov_b32_e32 v159, 0
	s_waitcnt lgkmcnt(1)
	v_add_f32_e32 v6, v10, v6
	v_mul_f32_e32 v11, 0x3e4ccccd, v6
	v_max_f32_e32 v11, v6, v11
	v_add_f32_e32 v6, v10, v7
	v_mul_f32_e32 v7, 0x3e4ccccd, v6
	v_max_f32_e32 v12, v6, v7
	v_add_f32_e32 v6, v10, v8
	v_mul_f32_e32 v7, 0x3e4ccccd, v6
	v_max_f32_e32 v13, v6, v7
	v_add_f32_e32 v6, v10, v9
	v_mul_f32_e32 v7, 0x3e4ccccd, v6
	s_waitcnt lgkmcnt(0)
	v_add_f32_e32 v2, v10, v2
	v_max_f32_e32 v14, v6, v7
	v_mul_f32_e32 v6, 0x3e4ccccd, v2
	v_max_f32_e32 v15, v2, v6
	v_add_f32_e32 v2, v10, v3
	v_mul_f32_e32 v3, 0x3e4ccccd, v2
	ds_read_b128 v[6:9], v91 offset:64
	v_max_f32_e32 v16, v2, v3
	v_add_f32_e32 v2, v10, v4
	v_mul_f32_e32 v3, 0x3e4ccccd, v2
	v_max_f32_e32 v17, v2, v3
	v_add_f32_e32 v2, v10, v5
	v_mul_f32_e32 v3, 0x3e4ccccd, v2
	v_max_f32_e32 v20, v2, v3
	ds_read_b128 v[2:5], v91 offset:96
	s_waitcnt lgkmcnt(1)
	v_add_f32_e32 v6, v10, v6
	v_mul_f32_e32 v18, 0x3e4ccccd, v6
	v_max_f32_e32 v22, v6, v18
	v_add_f32_e32 v6, v10, v7
	v_mul_f32_e32 v7, 0x3e4ccccd, v6
	v_max_f32_e32 v23, v6, v7
	v_add_f32_e32 v6, v10, v8
	v_mul_f32_e32 v7, 0x3e4ccccd, v6
	v_max_f32_e32 v24, v6, v7
	v_add_f32_e32 v6, v10, v9
	v_mul_f32_e32 v7, 0x3e4ccccd, v6
	s_waitcnt lgkmcnt(0)
	v_add_f32_e32 v2, v10, v2
	v_max_f32_e32 v25, v6, v7
	v_mul_f32_e32 v6, 0x3e4ccccd, v2
	v_max_f32_e32 v26, v2, v6
	v_add_f32_e32 v2, v10, v3
	v_mul_f32_e32 v3, 0x3e4ccccd, v2
	ds_read_b128 v[6:9], v91 offset:128
	v_max_f32_e32 v27, v2, v3
	v_add_f32_e32 v2, v10, v4
	v_mul_f32_e32 v3, 0x3e4ccccd, v2
	v_max_f32_e32 v28, v2, v3
	v_add_f32_e32 v2, v10, v5
	v_mul_f32_e32 v3, 0x3e4ccccd, v2
	v_max_f32_e32 v29, v2, v3
	ds_read_b128 v[2:5], v91 offset:160
	s_waitcnt lgkmcnt(1)
	v_add_f32_e32 v6, v10, v6
	v_mul_f32_e32 v18, 0x3e4ccccd, v6
	v_max_f32_e32 v30, v6, v18
	v_add_f32_e32 v6, v10, v7
	v_mul_f32_e32 v7, 0x3e4ccccd, v6
	v_max_f32_e32 v31, v6, v7
	v_add_f32_e32 v6, v10, v8
	v_mul_f32_e32 v7, 0x3e4ccccd, v6
	v_max_f32_e32 v32, v6, v7
	v_add_f32_e32 v6, v10, v9
	v_mul_f32_e32 v7, 0x3e4ccccd, v6
	s_waitcnt lgkmcnt(0)
	v_add_f32_e32 v2, v10, v2
	v_max_f32_e32 v33, v6, v7
	v_mul_f32_e32 v6, 0x3e4ccccd, v2
	v_max_f32_e32 v40, v2, v6
	v_add_f32_e32 v2, v10, v3
	v_mul_f32_e32 v3, 0x3e4ccccd, v2
	ds_read_b128 v[6:9], v91 offset:192
	v_max_f32_e32 v41, v2, v3
	v_add_f32_e32 v2, v10, v4
	v_mul_f32_e32 v3, 0x3e4ccccd, v2
	v_max_f32_e32 v42, v2, v3
	v_add_f32_e32 v2, v10, v5
	v_mul_f32_e32 v3, 0x3e4ccccd, v2
	v_max_f32_e32 v43, v2, v3
	ds_read_b128 v[2:5], v91 offset:224
	s_waitcnt lgkmcnt(1)
	v_add_f32_e32 v6, v10, v6
	v_mul_f32_e32 v18, 0x3e4ccccd, v6
	v_max_f32_e32 v44, v6, v18
	v_add_f32_e32 v6, v10, v7
	v_mul_f32_e32 v7, 0x3e4ccccd, v6
	v_max_f32_e32 v45, v6, v7
	v_add_f32_e32 v6, v10, v8
	v_mul_f32_e32 v7, 0x3e4ccccd, v6
	v_max_f32_e32 v46, v6, v7
	v_add_f32_e32 v6, v10, v9
	v_mul_f32_e32 v7, 0x3e4ccccd, v6
	s_waitcnt lgkmcnt(0)
	v_add_f32_e32 v2, v10, v2
	v_max_f32_e32 v47, v6, v7
	v_mul_f32_e32 v6, 0x3e4ccccd, v2
	v_max_f32_e32 v48, v2, v6
	v_add_f32_e32 v2, v10, v3
	v_mul_f32_e32 v3, 0x3e4ccccd, v2
	ds_read_b128 v[6:9], v91 offset:256
	v_max_f32_e32 v49, v2, v3
	v_add_f32_e32 v2, v10, v4
	v_mul_f32_e32 v3, 0x3e4ccccd, v2
	v_max_f32_e32 v50, v2, v3
	v_add_f32_e32 v2, v10, v5
	v_mul_f32_e32 v3, 0x3e4ccccd, v2
	v_max_f32_e32 v51, v2, v3
	ds_read_b128 v[2:5], v91 offset:288
	s_waitcnt lgkmcnt(1)
	v_add_f32_e32 v6, v10, v6
	v_mul_f32_e32 v18, 0x3e4ccccd, v6
	v_max_f32_e32 v52, v6, v18
	v_add_f32_e32 v6, v10, v7
	v_mul_f32_e32 v7, 0x3e4ccccd, v6
	v_max_f32_e32 v53, v6, v7
	v_add_f32_e32 v6, v10, v8
	v_mul_f32_e32 v7, 0x3e4ccccd, v6
	v_max_f32_e32 v54, v6, v7
	v_add_f32_e32 v6, v10, v9
	v_mul_f32_e32 v7, 0x3e4ccccd, v6
	s_waitcnt lgkmcnt(0)
	v_add_f32_e32 v2, v10, v2
	v_max_f32_e32 v55, v6, v7
	v_mul_f32_e32 v6, 0x3e4ccccd, v2
	v_max_f32_e32 v56, v2, v6
	v_add_f32_e32 v2, v10, v3
	v_mul_f32_e32 v3, 0x3e4ccccd, v2
	ds_read_b128 v[6:9], v91 offset:320
	v_max_f32_e32 v57, v2, v3
	v_add_f32_e32 v2, v10, v4
	v_mul_f32_e32 v3, 0x3e4ccccd, v2
	v_max_f32_e32 v92, v2, v3
	v_add_f32_e32 v2, v10, v5
	v_mul_f32_e32 v3, 0x3e4ccccd, v2
	v_max_f32_e32 v94, v2, v3
	ds_read_b128 v[2:5], v91 offset:352
	s_waitcnt lgkmcnt(1)
	v_add_f32_e32 v6, v10, v6
	v_mul_f32_e32 v18, 0x3e4ccccd, v6
	v_max_f32_e32 v95, v6, v18
	v_add_f32_e32 v6, v10, v7
	v_mul_f32_e32 v7, 0x3e4ccccd, v6
	v_max_f32_e32 v96, v6, v7
	v_add_f32_e32 v6, v10, v8
	v_mul_f32_e32 v7, 0x3e4ccccd, v6
	v_max_f32_e32 v97, v6, v7
	v_add_f32_e32 v6, v10, v9
	v_mul_f32_e32 v7, 0x3e4ccccd, v6
	s_waitcnt lgkmcnt(0)
	v_add_f32_e32 v2, v10, v2
	v_max_f32_e32 v98, v6, v7
	v_mul_f32_e32 v6, 0x3e4ccccd, v2
	v_max_f32_e32 v99, v2, v6
	v_add_f32_e32 v2, v10, v3
	v_mul_f32_e32 v3, 0x3e4ccccd, v2
	ds_read_b128 v[6:9], v91 offset:384
	v_max_f32_e32 v100, v2, v3
	v_add_f32_e32 v2, v10, v4
	v_mul_f32_e32 v3, 0x3e4ccccd, v2
	v_max_f32_e32 v101, v2, v3
	v_add_f32_e32 v2, v10, v5
	v_mul_f32_e32 v3, 0x3e4ccccd, v2
	v_max_f32_e32 v102, v2, v3
	ds_read_b128 v[2:5], v91 offset:416
	s_waitcnt lgkmcnt(1)
	v_add_f32_e32 v6, v10, v6
	v_mul_f32_e32 v18, 0x3e4ccccd, v6
	v_max_f32_e32 v103, v6, v18
	v_add_f32_e32 v6, v10, v7
	v_mul_f32_e32 v7, 0x3e4ccccd, v6
	v_max_f32_e32 v104, v6, v7
	v_add_f32_e32 v6, v10, v8
	v_mul_f32_e32 v7, 0x3e4ccccd, v6
	v_max_f32_e32 v105, v6, v7
	v_add_f32_e32 v6, v10, v9
	v_mul_f32_e32 v7, 0x3e4ccccd, v6
	s_waitcnt lgkmcnt(0)
	v_add_f32_e32 v2, v10, v2
	v_max_f32_e32 v106, v6, v7
	v_mul_f32_e32 v6, 0x3e4ccccd, v2
	v_max_f32_e32 v107, v2, v6
	v_add_f32_e32 v2, v10, v3
	v_mul_f32_e32 v3, 0x3e4ccccd, v2
	ds_read_b128 v[6:9], v91 offset:448
	v_max_f32_e32 v108, v2, v3
	v_add_f32_e32 v2, v10, v4
	v_mul_f32_e32 v3, 0x3e4ccccd, v2
	v_max_f32_e32 v109, v2, v3
	v_add_f32_e32 v2, v10, v5
	v_mul_f32_e32 v3, 0x3e4ccccd, v2
	v_max_f32_e32 v110, v2, v3
	ds_read_b128 v[2:5], v91 offset:480
	s_waitcnt lgkmcnt(1)
	v_add_f32_e32 v6, v10, v6
	v_mul_f32_e32 v18, 0x3e4ccccd, v6
	v_max_f32_e32 v111, v6, v18
	v_add_f32_e32 v6, v10, v7
	v_mul_f32_e32 v7, 0x3e4ccccd, v6
	v_max_f32_e32 v114, v6, v7
	v_add_f32_e32 v6, v10, v8
	v_mul_f32_e32 v7, 0x3e4ccccd, v6
	v_max_f32_e32 v115, v6, v7
	v_add_f32_e32 v6, v10, v9
	v_mul_f32_e32 v7, 0x3e4ccccd, v6
	s_waitcnt lgkmcnt(0)
	v_add_f32_e32 v2, v10, v2
	v_max_f32_e32 v116, v6, v7
	v_mul_f32_e32 v6, 0x3e4ccccd, v2
	v_max_f32_e32 v117, v2, v6
	v_add_f32_e32 v2, v10, v3
	v_mul_f32_e32 v3, 0x3e4ccccd, v2
	v_max_f32_e32 v120, v2, v3
	v_add_f32_e32 v2, v10, v4
	v_mul_f32_e32 v3, 0x3e4ccccd, v2
	v_max_f32_e32 v121, v2, v3
	v_add_f32_e32 v2, v10, v5
	v_mul_f32_e32 v3, 0x3e4ccccd, v2
	v_max_f32_e32 v122, v2, v3
	s_nop 1
	v_exp_f32_e32 v2, v11
	v_exp_f32_e32 v3, v12
	v_exp_f32_e32 v4, v14
	v_cvt_pkrtz_f16_f32 v2, v2, v3
	v_exp_f32_e32 v3, v13
	v_and_b32_e32 v18, v127, v2
	v_exp_f32_e32 v5, v20
	v_cvt_pkrtz_f16_f32 v2, v3, v4
	v_and_b32_e32 v19, v128, v2
	v_exp_f32_e32 v2, v15
	v_exp_f32_e32 v3, v16
	v_exp_f32_e32 v4, v17
	v_dot2c_f32_f16_e32 v159, 0x3c003c00, v18
	v_cvt_pkrtz_f16_f32 v2, v2, v3
	v_and_b32_e32 v20, v129, v2
	v_cvt_pkrtz_f16_f32 v2, v4, v5
	v_and_b32_e32 v21, v130, v2
	v_exp_f32_e32 v2, v22
	v_exp_f32_e32 v3, v23
	v_exp_f32_e32 v4, v24
	v_exp_f32_e32 v5, v25
	v_cvt_pkrtz_f16_f32 v2, v2, v3
	v_and_b32_e32 v34, v131, v2
	v_cvt_pkrtz_f16_f32 v2, v4, v5
	v_and_b32_e32 v35, v132, v2
	v_exp_f32_e32 v2, v26
	v_exp_f32_e32 v3, v27
	v_exp_f32_e32 v4, v28
	v_exp_f32_e32 v5, v29
	v_cvt_pkrtz_f16_f32 v2, v2, v3
	v_and_b32_e32 v36, v133, v2
	v_cvt_pkrtz_f16_f32 v2, v4, v5
	v_and_b32_e32 v37, v134, v2
	v_exp_f32_e32 v2, v30
	v_exp_f32_e32 v3, v31
	v_exp_f32_e32 v4, v32
	v_exp_f32_e32 v5, v33
	v_cvt_pkrtz_f16_f32 v2, v2, v3
	v_and_b32_e32 v38, v135, v2
	v_cvt_pkrtz_f16_f32 v2, v4, v5
	v_and_b32_e32 v39, v136, v2
	v_exp_f32_e32 v2, v40
	v_exp_f32_e32 v3, v41
	v_exp_f32_e32 v4, v42
	v_exp_f32_e32 v5, v43
	v_cvt_pkrtz_f16_f32 v2, v2, v3
	v_and_b32_e32 v40, v137, v2
	v_cvt_pkrtz_f16_f32 v2, v4, v5
	v_and_b32_e32 v41, v138, v2
	v_exp_f32_e32 v2, v44
	v_exp_f32_e32 v3, v45
	v_exp_f32_e32 v4, v46
	v_exp_f32_e32 v5, v47
	v_cvt_pkrtz_f16_f32 v2, v2, v3
	v_and_b32_e32 v42, v139, v2
	v_cvt_pkrtz_f16_f32 v2, v4, v5
	v_and_b32_e32 v43, v140, v2
	v_exp_f32_e32 v2, v48
	v_exp_f32_e32 v3, v49
	v_exp_f32_e32 v4, v50
	v_exp_f32_e32 v5, v51
	v_cvt_pkrtz_f16_f32 v2, v2, v3
	v_and_b32_e32 v44, v141, v2
	v_cvt_pkrtz_f16_f32 v2, v4, v5
	v_and_b32_e32 v45, v142, v2
	v_exp_f32_e32 v2, v52
	v_exp_f32_e32 v3, v53
	v_exp_f32_e32 v4, v54
	v_exp_f32_e32 v5, v55
	v_cvt_pkrtz_f16_f32 v2, v2, v3
	v_and_b32_e32 v46, v143, v2
	v_cvt_pkrtz_f16_f32 v2, v4, v5
	v_and_b32_e32 v47, v144, v2
	v_exp_f32_e32 v2, v56
	v_exp_f32_e32 v3, v57
	v_exp_f32_e32 v4, v92
	v_exp_f32_e32 v5, v94
	v_cvt_pkrtz_f16_f32 v2, v2, v3
	v_and_b32_e32 v48, v145, v2
	v_cvt_pkrtz_f16_f32 v2, v4, v5
	v_and_b32_e32 v49, v146, v2
	v_exp_f32_e32 v2, v95
	v_exp_f32_e32 v3, v96
	v_exp_f32_e32 v4, v97
	v_exp_f32_e32 v5, v98
	v_cvt_pkrtz_f16_f32 v2, v2, v3
	v_and_b32_e32 v50, v147, v2
	v_cvt_pkrtz_f16_f32 v2, v4, v5
	v_and_b32_e32 v51, v148, v2
	v_exp_f32_e32 v2, v99
	v_exp_f32_e32 v3, v100
	v_exp_f32_e32 v4, v101
	v_exp_f32_e32 v5, v102
	v_cvt_pkrtz_f16_f32 v2, v2, v3
	v_and_b32_e32 v52, v149, v2
	v_cvt_pkrtz_f16_f32 v2, v4, v5
	v_and_b32_e32 v53, v150, v2
	v_exp_f32_e32 v2, v103
	v_exp_f32_e32 v3, v104
	v_exp_f32_e32 v4, v105
	v_exp_f32_e32 v5, v106
	v_cvt_pkrtz_f16_f32 v2, v2, v3
	v_and_b32_e32 v54, v151, v2
	v_exp_f32_e32 v26, v107
	v_cvt_pkrtz_f16_f32 v2, v4, v5
	v_and_b32_e32 v55, v152, v2
	ds_read_b128 v[2:5], v113
	ds_read_b128 v[22:25], v113 offset:32
	v_exp_f32_e32 v27, v108
	v_exp_f32_e32 v28, v109
	s_waitcnt lgkmcnt(1)
	v_mfma_f32_32x32x16_f16 v[2:17], v[2:5], v[18:21], 0
	v_exp_f32_e32 v29, v110
	v_cvt_pkrtz_f16_f32 v26, v26, v27
	v_and_b32_e32 v56, v153, v26
	v_dot2c_f32_f16_e32 v159, 0x3c003c00, v19
	v_cvt_pkrtz_f16_f32 v30, v28, v29
	ds_read_b128 v[26:29], v113 offset:64
	s_waitcnt lgkmcnt(1)
	v_mfma_f32_32x32x16_f16 v[2:17], v[22:25], v[34:37], v[2:17]
	v_and_b32_e32 v57, v154, v30
	v_exp_f32_e32 v30, v111
	v_exp_f32_e32 v31, v114
	ds_read_b128 v[22:25], v113 offset:96
	v_dot2c_f32_f16_e32 v159, 0x3c003c00, v20
	s_waitcnt lgkmcnt(1)
	v_mfma_f32_32x32x16_f16 v[2:17], v[26:29], v[38:41], v[2:17]
	v_cvt_pkrtz_f16_f32 v26, v30, v31
	v_and_b32_e32 v100, v155, v26
	v_exp_f32_e32 v30, v115
	v_exp_f32_e32 v31, v116
	ds_read_b128 v[26:29], v113 offset:128
	s_waitcnt lgkmcnt(1)
	v_mfma_f32_32x32x16_f16 v[2:17], v[22:25], v[42:45], v[2:17]
	v_dot2c_f32_f16_e32 v159, 0x3c003c00, v21
	v_dot2c_f32_f16_e32 v159, 0x3c003c00, v34
	v_dot2c_f32_f16_e32 v159, 0x3c003c00, v35
	v_cvt_pkrtz_f16_f32 v22, v30, v31
	v_dot2c_f32_f16_e32 v159, 0x3c003c00, v36
	v_and_b32_e32 v101, v156, v22
	v_dot2c_f32_f16_e32 v159, 0x3c003c00, v37
	v_exp_f32_e32 v30, v117
	ds_read_b128 v[22:25], v113 offset:160
	v_dot2c_f32_f16_e32 v159, 0x3c003c00, v38
	s_waitcnt lgkmcnt(1)
	v_mfma_f32_32x32x16_f16 v[2:17], v[26:29], v[46:49], v[2:17]
	v_dot2c_f32_f16_e32 v159, 0x3c003c00, v39
	v_dot2c_f32_f16_e32 v159, 0x3c003c00, v40
	v_dot2c_f32_f16_e32 v159, 0x3c003c00, v41
	v_dot2c_f32_f16_e32 v159, 0x3c003c00, v42
	v_dot2c_f32_f16_e32 v159, 0x3c003c00, v43
	v_exp_f32_e32 v31, v120
	v_dot2c_f32_f16_e32 v159, 0x3c003c00, v44
	v_exp_f32_e32 v32, v121
	v_dot2c_f32_f16_e32 v159, 0x3c003c00, v45
	v_exp_f32_e32 v33, v122
	ds_read_b128 v[26:29], v113 offset:192
	v_dot2c_f32_f16_e32 v159, 0x3c003c00, v46
	s_waitcnt lgkmcnt(1)
	v_mfma_f32_32x32x16_f16 v[2:17], v[22:25], v[50:53], v[2:17]
	v_dot2c_f32_f16_e32 v159, 0x3c003c00, v47
	v_dot2c_f32_f16_e32 v159, 0x3c003c00, v48
	v_dot2c_f32_f16_e32 v159, 0x3c003c00, v49
	v_dot2c_f32_f16_e32 v159, 0x3c003c00, v50
	v_dot2c_f32_f16_e32 v159, 0x3c003c00, v51
	v_cvt_pkrtz_f16_f32 v22, v30, v31
	v_dot2c_f32_f16_e32 v159, 0x3c003c00, v52
	v_and_b32_e32 v102, v157, v22
	v_cvt_pkrtz_f16_f32 v22, v32, v33
	v_dot2c_f32_f16_e32 v159, 0x3c003c00, v53
	v_and_b32_e32 v103, v158, v22
	ds_read_b128 v[22:25], v113 offset:224
	v_dot2c_f32_f16_e32 v159, 0x3c003c00, v54
	s_waitcnt lgkmcnt(1)
	v_mfma_f32_32x32x16_f16 v[2:17], v[26:29], v[54:57], v[2:17]
	v_dot2c_f32_f16_e32 v159, 0x3c003c00, v55
	v_dot2c_f32_f16_e32 v159, 0x3c003c00, v56
	v_dot2c_f32_f16_e32 v159, 0x3c003c00, v57
	v_dot2c_f32_f16_e32 v159, 0x3c003c00, v100
	v_dot2c_f32_f16_e32 v159, 0x3c003c00, v101
	v_dot2c_f32_f16_e32 v159, 0x3c003c00, v102
	v_dot2c_f32_f16_e32 v159, 0x3c003c00, v103
	s_waitcnt lgkmcnt(0)
	v_mfma_f32_32x32x16_f16 v[2:17], v[22:25], v[100:103], v[2:17]
	s_xor_b64 s[14:15], s[4:5], -1
	s_mov_b32 s17, 1
	v_mov_b32_e32 v26, v159
	v_mov_b32_e32 v27, v159
	s_nop 1
	v_permlane32_swap_b32_e32 v26, v27
	v_cndmask_b32_e64 v26, v26, v27, s[2:3]
	v_add_f32_e32 v26, v159, v26
	v_rcp_f32_e32 v92, v26
	s_mov_b64 s[4:5], 0
	s_nop 0
	v_pk_mul_f32 v[2:3], v[92:93], v[2:3] op_sel_hi:[0,1]
	v_mul_f32_e32 v22, 0x3fb8aa3b, v2
	v_mul_f32_e32 v23, 0x3fb8aa3b, v3
	v_exp_f32_e32 v22, v22
	v_exp_f32_e32 v23, v23
	v_pk_mul_f32 v[24:25], v[92:93], v[4:5] op_sel_hi:[0,1]
	v_mul_f32_e32 v4, 0x3fb8aa3b, v24
	v_mul_f32_e32 v5, 0x3fb8aa3b, v25
	v_pk_add_f32 v[22:23], v[22:23], -1.0 op_sel_hi:[1,0]
	v_exp_f32_e32 v4, v4
	v_exp_f32_e32 v5, v5
	v_pk_mul_f32 v[104:105], v[92:93], v[6:7] op_sel_hi:[0,1]
	v_pk_mul_f32 v[108:109], v[92:93], v[8:9] op_sel_hi:[0,1]
	v_med3_f32 v94, v3, v23, 0
	v_pk_mul_f32 v[10:11], v[92:93], v[10:11] op_sel_hi:[0,1]
	v_pk_mul_f32 v[12:13], v[92:93], v[12:13] op_sel_hi:[0,1]
	v_med3_f32 v95, v2, v22, 0
	v_mul_f32_e32 v2, 0x3fb8aa3b, v104
	v_exp_f32_e32 v6, v2
	v_mul_f32_e32 v2, 0x3fb8aa3b, v105
	v_pk_add_f32 v[22:23], v[4:5], -1.0 op_sel_hi:[1,0]
	v_exp_f32_e32 v7, v2
	ds_read_b128 v[2:5], v113 offset:8704
	v_pk_mul_f32 v[14:15], v[92:93], v[14:15] op_sel_hi:[0,1]
	v_pk_add_f32 v[106:107], v[6:7], -1.0 op_sel_hi:[1,0]
	v_mul_f32_e32 v6, 0x3fb8aa3b, v108
	v_med3_f32 v96, v25, v23, 0
	v_exp_f32_e32 v110, v6
	ds_read_b128 v[6:9], v113 offset:8736
	v_med3_f32 v97, v24, v22, 0
	s_waitcnt lgkmcnt(1)
	v_mfma_f32_32x32x16_f16 v[18:33], v[2:5], v[18:21], 0
	v_mul_f32_e32 v2, 0x3fb8aa3b, v109
	v_exp_f32_e32 v111, v2
	ds_read_b128 v[2:5], v113 offset:8768
	v_med3_f32 v98, v105, v107, 0
	s_waitcnt lgkmcnt(1)
	v_mfma_f32_32x32x16_f16 v[18:33], v[6:9], v[34:37], v[18:33]
	v_mul_f32_e32 v6, 0x3fb8aa3b, v10
	v_exp_f32_e32 v36, v6
	v_mul_f32_e32 v6, 0x3fb8aa3b, v11
	v_exp_f32_e32 v37, v6
	ds_read_b128 v[6:9], v113 offset:8800
	v_cmp_lt_f32_e32 vcc, 0, v104
	s_waitcnt lgkmcnt(1)
	v_mfma_f32_32x32x16_f16 v[18:33], v[2:5], v[38:41], v[18:33]
	v_mul_f32_e32 v2, 0x3fb8aa3b, v12
	v_exp_f32_e32 v40, v2
	ds_read_b128 v[2:5], v113 offset:8832
	v_add_f32_e32 v38, -1.0, v36
	v_add_f32_e32 v39, -1.0, v37
	v_mul_f32_e32 v36, 0x3fb8aa3b, v13
	v_cndmask_b32_e32 v99, v106, v104, vcc
	v_add_f32_e32 v104, -1.0, v110
	v_add_f32_e32 v105, -1.0, v111
	s_waitcnt lgkmcnt(1)
	v_mfma_f32_32x32x16_f16 v[18:33], v[6:9], v[42:45], v[18:33]
	ds_read_b128 v[6:9], v113 offset:8864
	v_exp_f32_e32 v41, v36
	v_med3_f32 v34, v109, v105, 0
	s_waitcnt lgkmcnt(1)
	v_mfma_f32_32x32x16_f16 v[18:33], v[2:5], v[46:49], v[18:33]
	v_med3_f32 v35, v108, v104, 0
	v_mul_f32_e32 v2, 0x3fb8aa3b, v14
	v_med3_f32 v36, v11, v39, 0
	s_waitcnt lgkmcnt(0)
	v_mfma_f32_32x32x16_f16 v[18:33], v[6:9], v[50:53], v[18:33]
	v_med3_f32 v37, v10, v38, 0
	v_add_f32_e64 v10, v40, -1.0
	v_add_f32_e64 v11, v41, -1.0
	v_exp_f32_e32 v40, v2
	v_mul_f32_e32 v2, 0x3fb8aa3b, v15
	v_exp_f32_e32 v41, v2
	ds_read_b128 v[2:5], v113 offset:8896
	v_med3_f32 v38, v13, v11, 0
	v_med3_f32 v39, v12, v10, 0
	v_pk_mul_f32 v[12:13], v[92:93], v[16:17] op_sel_hi:[0,1]
	v_mul_f32_e32 v6, 0x3fb8aa3b, v12
	v_exp_f32_e32 v16, v6
	ds_read_b128 v[6:9], v113 offset:8928
	s_waitcnt lgkmcnt(1)
	v_mfma_f32_32x32x16_f16 v[18:33], v[2:5], v[54:57], v[18:33]
	v_mul_f32_e32 v2, 0x3fb8aa3b, v13
	v_exp_f32_e32 v17, v2
	v_add_f32_e32 v10, -1.0, v40
	v_add_f32_e32 v11, -1.0, v41
	s_waitcnt lgkmcnt(0)
	v_add_f32_e32 v2, -1.0, v16
	v_add_f32_e32 v3, -1.0, v17
	v_med3_f32 v40, v15, v11, 0
	v_mfma_f32_32x32x16_f16 v[18:33], v[6:9], v[100:103], v[18:33]
	s_barrier
	v_med3_f32 v41, v14, v10, 0
	s_nop 9
	v_pk_mul_f32 v[4:5], v[92:93], v[18:19] op_sel_hi:[0,1]
	v_mul_f32_e32 v6, 0x3fb8aa3b, v4
	v_mul_f32_e32 v7, 0x3fb8aa3b, v5
	v_exp_f32_e32 v6, v6
	v_exp_f32_e32 v7, v7
	s_nop 4
	v_med3_f32 v18, v13, v3, 0
	s_nop 3
	v_med3_f32 v19, v12, v2, 0
	v_pk_add_f32 v[2:3], v[6:7], -1.0 op_sel_hi:[1,0]
	s_nop 1
	v_pk_mul_f32 v[6:7], v[92:93], v[20:21] op_sel_hi:[0,1]
	v_mul_f32_e32 v8, 0x3fb8aa3b, v6
	v_mul_f32_e32 v9, 0x3fb8aa3b, v7
	v_exp_f32_e32 v8, v8
	v_exp_f32_e32 v9, v9
	v_med3_f32 v20, v5, v3, 0
	v_med3_f32 v21, v4, v2, 0
	v_pk_mul_f32 v[4:5], v[92:93], v[22:23] op_sel_hi:[0,1]
	v_pk_add_f32 v[2:3], v[8:9], -1.0 op_sel_hi:[1,0]
	v_mul_f32_e32 v8, 0x3fb8aa3b, v4
	v_mul_f32_e32 v9, 0x3fb8aa3b, v5
	v_exp_f32_e32 v8, v8
	v_exp_f32_e32 v9, v9
	v_med3_f32 v22, v7, v3, 0
	v_med3_f32 v23, v6, v2, 0
	v_pk_mul_f32 v[6:7], v[92:93], v[24:25] op_sel_hi:[0,1]
	v_pk_add_f32 v[2:3], v[8:9], -1.0 op_sel_hi:[1,0]
	v_mul_f32_e32 v8, 0x3fb8aa3b, v6
	v_mul_f32_e32 v9, 0x3fb8aa3b, v7
	v_exp_f32_e32 v8, v8
	v_exp_f32_e32 v9, v9
	v_med3_f32 v24, v5, v3, 0
	v_med3_f32 v42, v4, v2, 0
	v_pk_mul_f32 v[4:5], v[92:93], v[26:27] op_sel_hi:[0,1]
	v_pk_add_f32 v[2:3], v[8:9], -1.0 op_sel_hi:[1,0]
	v_mul_f32_e32 v8, 0x3fb8aa3b, v4
	v_mul_f32_e32 v9, 0x3fb8aa3b, v5
	v_exp_f32_e32 v8, v8
	v_exp_f32_e32 v9, v9
	v_med3_f32 v27, v7, v3, 0
	v_med3_f32 v43, v6, v2, 0
	v_pk_mul_f32 v[6:7], v[92:93], v[28:29] op_sel_hi:[0,1]
	v_pk_add_f32 v[2:3], v[8:9], -1.0 op_sel_hi:[1,0]
	v_mul_f32_e32 v8, 0x3fb8aa3b, v6
	v_mul_f32_e32 v9, 0x3fb8aa3b, v7
	v_exp_f32_e32 v8, v8
	v_exp_f32_e32 v9, v9
	v_med3_f32 v25, v5, v3, 0
	v_med3_f32 v26, v4, v2, 0
	v_pk_mul_f32 v[4:5], v[92:93], v[30:31] op_sel_hi:[0,1]
	v_pk_add_f32 v[2:3], v[8:9], -1.0 op_sel_hi:[1,0]
	v_mul_f32_e32 v8, 0x3fb8aa3b, v4
	v_mul_f32_e32 v9, 0x3fb8aa3b, v5
	v_exp_f32_e32 v8, v8
	v_exp_f32_e32 v9, v9
	v_med3_f32 v28, v7, v3, 0
	v_med3_f32 v29, v6, v2, 0
	v_pk_mul_f32 v[6:7], v[92:93], v[32:33] op_sel_hi:[0,1]
	v_pk_add_f32 v[2:3], v[8:9], -1.0 op_sel_hi:[1,0]
	v_mul_f32_e32 v8, 0x3fb8aa3b, v6
	v_mul_f32_e32 v9, 0x3fb8aa3b, v7
	v_exp_f32_e32 v8, v8
	v_exp_f32_e32 v9, v9
	v_med3_f32 v30, v5, v3, 0
	v_med3_f32 v32, v4, v2, 0
	v_pk_add_f32 v[2:3], v[8:9], -1.0 op_sel_hi:[1,0]
	v_med3_f32 v31, v7, v3, 0
	v_med3_f32 v33, v6, v2, 0
	s_and_b64 vcc, exec, s[14:15]
	s_cbranch_vccnz .LBB2_97

.LBB2_97:
	ds_read_b128 v[2:5], v125 offset:40960
	ds_read_b128 v[48:51], v125 offset:41984
	v_cvt_pkrtz_f16_f32 v44, v95, v94
	v_cvt_pkrtz_f16_f32 v45, v97, v96
	v_cvt_pkrtz_f16_f32 v46, v99, v98
	v_cvt_pkrtz_f16_f32 v47, v35, v34
	v_cvt_pkrtz_f16_f32 v34, v37, v36
	v_cvt_pkrtz_f16_f32 v35, v39, v38
	v_cvt_pkrtz_f16_f32 v36, v41, v40
	s_waitcnt lgkmcnt(1)
	v_mfma_f32_32x32x16_f16 v[2:17], v[2:5], v[44:47], 0
	v_cvt_pkrtz_f16_f32 v37, v19, v18
	ds_read_b128 v[38:41], v125 offset:43008
	v_add_u32_e32 v92, 0, v90
	s_mov_b32 s4, 0xff61b1e6
	v_mov_b32_e32 v91, 0
	s_waitcnt lgkmcnt(1)
	v_mfma_f32_32x32x16_f16 v[2:17], v[48:51], v[34:37], v[2:17]
	v_cvt_pkrtz_f16_f32 v48, v21, v20
	v_cvt_pkrtz_f16_f32 v49, v23, v22
	v_cvt_pkrtz_f16_f32 v50, v42, v24
	v_cvt_pkrtz_f16_f32 v51, v43, v27
	ds_read_b128 v[18:21], v125 offset:44032
	s_waitcnt lgkmcnt(1)
	v_mfma_f32_32x32x16_f16 v[2:17], v[38:41], v[48:51], v[2:17]
	v_cvt_pkrtz_f16_f32 v38, v26, v25
	v_cvt_pkrtz_f16_f32 v39, v29, v28
	v_cvt_pkrtz_f16_f32 v40, v32, v30
	v_cvt_pkrtz_f16_f32 v41, v33, v31
	s_waitcnt lgkmcnt(0)
	s_nop 0
	v_mfma_f32_32x32x16_f16 v[2:17], v[18:21], v[38:41], v[2:17]
	ds_read_b128 v[18:21], v125 offset:45056
	ds_read_b128 v[52:55], v125 offset:46080
	ds_read_b128 v[94:97], v92 offset:62464
	ds_read_b128 v[98:101], v125 offset:47104
	ds_read_b128 v[102:105], v125 offset:48128
	s_waitcnt lgkmcnt(2)
	s_nop 5
	v_add_f32_e32 v56, v4, v96
	v_mfma_f32_32x32x16_f16 v[18:33], v[18:21], v[44:47], 0
	ds_read_b128 v[42:45], v92 offset:62496
	ds_read_b128 v[106:109], v92 offset:62528
	v_add_f32_e32 v46, v2, v94
	v_add_f32_e32 v47, v3, v95
	v_add_f32_e32 v57, v5, v97
	ds_read_b128 v[2:5], v92 offset:62560
	s_waitcnt lgkmcnt(2)
	v_add_f32_e32 v42, v6, v42
	s_waitcnt lgkmcnt(1)
	v_add_f32_e32 v10, v10, v106
	v_mfma_f32_32x32x16_f16 v[18:33], v[52:55], v[34:37], v[18:33]
	v_add_f32_e32 v34, v7, v43
	v_add_f32_e32 v35, v8, v44
	v_add_f32_e32 v36, v9, v45
	s_waitcnt lgkmcnt(0)
	v_add_f32_e32 v14, v14, v2
	v_add_f32_e32 v15, v15, v3
	v_add_f32_e32 v16, v16, v4
	v_add_f32_e32 v17, v17, v5
	v_mfma_f32_32x32x16_f16 v[18:33], v[98:101], v[48:51], v[18:33]
	ds_read_b128 v[2:5], v92 offset:62592
	ds_read_b128 v[6:9], v92 offset:62624
	v_max_f32_e32 v37, 0, v42
	v_max_f32_e32 v34, 0, v34
	v_max_f32_e32 v35, 0, v35
	v_max_f32_e32 v36, 0, v36
	v_add_f32_e32 v11, v11, v107
	v_add_f32_e32 v12, v12, v108
	v_mfma_f32_32x32x16_f16 v[18:33], v[102:105], v[38:41], v[18:33]
	v_add_f32_e32 v13, v13, v109
	v_max_f32_e32 v38, 0, v10
	v_max_f32_e32 v39, 0, v11
	v_max_f32_e32 v40, 0, v12
	v_max_f32_e32 v41, 0, v13
	v_max_f32_e32 v42, 0, v14
	v_max_f32_e32 v43, 0, v15
	s_waitcnt lgkmcnt(1)
	s_nop 3
	v_add_f32_e32 v18, v18, v2
	v_add_f32_e32 v19, v19, v3
	v_add_f32_e32 v20, v20, v4
	v_add_f32_e32 v21, v21, v5
	ds_read_b128 v[2:5], v92 offset:62656
	s_waitcnt lgkmcnt(1)
	v_add_f32_e32 v22, v22, v6
	v_add_f32_e32 v23, v23, v7
	v_add_f32_e32 v24, v24, v8
	v_add_f32_e32 v25, v25, v9
	ds_read_b128 v[6:9], v92 offset:62688
	s_waitcnt lgkmcnt(1)
	v_add_f32_e32 v26, v26, v2
	v_add_f32_e32 v27, v27, v3
	v_add_f32_e32 v28, v28, v4
	v_add_f32_e32 v29, v29, v5
	ds_read_b128 v[2:5], v125 offset:49152
	s_waitcnt lgkmcnt(1)
	v_add_f32_e32 v30, v30, v6
	v_add_f32_e32 v31, v31, v7
	v_add_f32_e32 v32, v32, v8
	v_add_f32_e32 v33, v33, v9
	v_max_f32_e32 v6, 0, v46
	v_max_f32_e32 v7, 0, v47
	v_max_f32_e32 v8, 0, v56
	v_max_f32_e32 v9, 0, v57
	v_max_f32_e32 v46, 0, v18
	v_max_f32_e32 v47, 0, v19
	v_max_f32_e32 v48, 0, v20
	v_max_f32_e32 v49, 0, v21
	v_cvt_pkrtz_f16_f32 v6, v6, v7
	v_cvt_pkrtz_f16_f32 v7, v8, v9
	v_cvt_pkrtz_f16_f32 v8, v37, v34
	v_cvt_pkrtz_f16_f32 v9, v35, v36
	ds_read_b128 v[18:21], v125 offset:50176
	v_max_f32_e32 v44, 0, v16
	v_max_f32_e32 v45, 0, v17
	s_waitcnt lgkmcnt(1)
	v_mfma_f32_32x32x16_f16 v[2:17], v[2:5], v[6:9], 0
	v_max_f32_e32 v50, 0, v22
	v_max_f32_e32 v51, 0, v23
	v_max_f32_e32 v52, 0, v24
	v_max_f32_e32 v53, 0, v25
	v_max_f32_e32 v54, 0, v26
	v_max_f32_e32 v55, 0, v27
	v_max_f32_e32 v34, 0, v28
	v_max_f32_e32 v35, 0, v29
	v_cvt_pkrtz_f16_f32 v22, v38, v39
	v_cvt_pkrtz_f16_f32 v23, v40, v41
	v_cvt_pkrtz_f16_f32 v24, v42, v43
	v_cvt_pkrtz_f16_f32 v25, v44, v45
	ds_read_b128 v[26:29], v125 offset:51200
	v_max_f32_e32 v30, 0, v30
	s_waitcnt lgkmcnt(1)
	v_mfma_f32_32x32x16_f16 v[2:17], v[18:21], v[22:25], v[2:17]
	v_cvt_pkrtz_f16_f32 v18, v46, v47
	v_cvt_pkrtz_f16_f32 v19, v48, v49
	v_cvt_pkrtz_f16_f32 v20, v50, v51
	v_cvt_pkrtz_f16_f32 v21, v52, v53
	ds_read_b128 v[22:25], v125 offset:52224
	v_max_f32_e32 v31, 0, v31
	s_waitcnt lgkmcnt(1)
	v_mfma_f32_32x32x16_f16 v[2:17], v[26:29], v[18:21], v[2:17]
	v_max_f32_e32 v21, 0, v32
	v_max_f32_e32 v26, 0, v33
	v_cvt_pkrtz_f16_f32 v18, v54, v55
	v_cvt_pkrtz_f16_f32 v19, v34, v35
	v_cvt_pkrtz_f16_f32 v20, v30, v31
	v_cvt_pkrtz_f16_f32 v21, v21, v26
	ds_read_b128 v[26:29], v92 offset:62720
	s_waitcnt lgkmcnt(1)
	v_mfma_f32_32x32x16_f16 v[2:17], v[22:25], v[18:21], v[2:17]
	s_nop 11
	ds_read_b128 v[10:13], v92 offset:62752
	s_waitcnt lgkmcnt(1)
	v_add_f32_e32 v2, v26, v2
	v_add_f32_e32 v3, v27, v3
	v_max3_f32 v15, v2, s4, v3
	v_add_f32_e32 v16, v28, v4
	v_add_f32_e32 v17, v29, v5
	v_max3_f32 v4, v15, v16, v17
	s_waitcnt lgkmcnt(0)
	v_add_f32_e32 v15, v10, v6
	v_add_f32_e32 v18, v11, v7
	v_max3_f32 v4, v4, v15, v18
	v_add_f32_e32 v12, v12, v8
	v_add_f32_e32 v13, v13, v9
	v_max3_f32 v4, v4, v12, v13
	v_mov_b32_e32 v5, v4
	v_mov_b32_e32 v6, v4
	s_nop 1
	v_permlane32_swap_b32_e32 v5, v6
	v_cndmask_b32_e64 v5, v5, v6, s[2:3]
	v_max_f32_e32 v5, v5, v5
	v_max_f32_e32 v19, v4, v5
	v_sub_f32_e32 v2, v2, v19
	v_mul_f32_e32 v2, 0x3fb8aa3b, v2
	v_exp_f32_e32 v10, v2
	v_sub_f32_e32 v2, v3, v19
	v_lshl_add_u32 v14, s28, 6, v92
	v_mul_f32_e32 v2, 0x3fb8aa3b, v2
	v_exp_f32_e32 v11, v2
	ds_read_b128 v[2:5], v14 offset:63808
	v_add_f32_e32 v6, 0, v10
	v_add_f32_e32 v20, v6, v11
	ds_read_b128 v[6:9], v14 offset:63840
	s_waitcnt lgkmcnt(1)
	v_pk_mul_f32 v[2:3], v[10:11], v[2:3]
	v_sub_f32_e32 v10, v16, v19
	v_mul_f32_e32 v10, 0x3fb8aa3b, v10
	v_sub_f32_e32 v11, v17, v19
	v_exp_f32_e32 v10, v10
	v_mul_f32_e32 v11, 0x3fb8aa3b, v11
	v_exp_f32_e32 v11, v11
	v_add_f32_e32 v2, 0, v2
	v_add_f32_e32 v14, v2, v3
	v_add_f32_e32 v2, v20, v10
	v_add_f32_e32 v16, v2, v11
	v_pk_mul_f32 v[2:3], v[10:11], v[4:5]
	v_sub_f32_e32 v4, v15, v19
	v_mul_f32_e32 v4, 0x3fb8aa3b, v4
	v_sub_f32_e32 v5, v18, v19
	v_exp_f32_e32 v4, v4
	v_mul_f32_e32 v5, 0x3fb8aa3b, v5
	v_exp_f32_e32 v5, v5
	v_add_f32_e32 v2, v14, v2
	v_add_f32_e32 v10, v2, v3
	v_add_f32_e32 v2, v16, v4
	v_add_f32_e32 v11, v2, v5
	s_waitcnt lgkmcnt(0)
	v_pk_mul_f32 v[2:3], v[4:5], v[6:7]
	v_sub_f32_e32 v4, v12, v19
	v_mul_f32_e32 v4, 0x3fb8aa3b, v4
	v_sub_f32_e32 v5, v13, v19
	v_exp_f32_e32 v4, v4
	v_mul_f32_e32 v5, 0x3fb8aa3b, v5
	v_exp_f32_e32 v5, v5
	v_add_f32_e32 v2, v10, v2
	v_add_f32_e32 v6, v2, v3
	v_add_f32_e32 v2, v11, v4
	v_add_f32_e32 v7, v2, v5
	v_pk_mul_f32 v[2:3], v[4:5], v[8:9]
	v_mov_b32_e32 v4, v7
	v_add_f32_e32 v2, v6, v2
	v_add_f32_e32 v2, v2, v3
	v_mov_b32_e32 v3, v7
	s_nop 1
	v_permlane32_swap_b32_e32 v3, v4
	v_cndmask_b32_e64 v3, v3, v4, s[2:3]
	v_add_f32_e32 v3, v7, v3
	v_mov_b32_e32 v4, v2
	v_mov_b32_e32 v5, v2
	v_rcp_f32_e32 v3, v3
	s_nop 0
	v_permlane32_swap_b32_e32 v4, v5
	v_cndmask_b32_e64 v4, v4, v5, s[2:3]
	v_add_f32_e32 v2, v2, v4
	v_mul_f32_e32 v14, v2, v3
	ds_read_b128 v[2:5], v125 offset:53248
	ds_read_b128 v[10:13], v125 offset:54272
	v_pk_add_f32 v[42:43], v[78:79], v[14:15] op_sel_hi:[1,0] neg_lo:[0,1] neg_hi:[0,1]
	v_pk_add_f32 v[44:45], v[80:81], v[14:15] op_sel_hi:[1,0] neg_lo:[0,1] neg_hi:[0,1]
	v_pk_add_f32 v[38:39], v[82:83], v[14:15] op_sel_hi:[1,0] neg_lo:[0,1] neg_hi:[0,1]
	v_pk_add_f32 v[40:41], v[84:85], v[14:15] op_sel_hi:[1,0] neg_lo:[0,1] neg_hi:[0,1]
	v_cvt_pkrtz_f16_f32 v6, v42, v43
	v_cvt_pkrtz_f16_f32 v7, v44, v45
	v_cvt_pkrtz_f16_f32 v8, v38, v39
	v_cvt_pkrtz_f16_f32 v9, v40, v41
	v_add_f32_e64 v34, v86, -v14
	v_add_f32_e64 v35, v87, -v14
	v_add_f32_e64 v36, v88, -v14
	v_add_f32_e64 v37, v89, -v14
	s_waitcnt lgkmcnt(1)
	v_mfma_f32_32x32x16_f16 v[18:33], v[2:5], v[6:9], 0
	v_add_f32_e64 v50, v72, -v14
	v_add_f32_e64 v51, v73, -v14
	v_add_f32_e64 v52, v74, -v14
	v_add_f32_e64 v53, v75, -v14
	v_add_f32_e64 v48, v68, -v14
	v_add_f32_e64 v49, v69, -v14
	v_pk_add_f32 v[54:55], v[70:71], v[14:15] op_sel_hi:[1,0] neg_lo:[0,1] neg_hi:[0,1]
	v_cvt_pkrtz_f16_f32 v68, v34, v35
	v_cvt_pkrtz_f16_f32 v69, v36, v37
	v_cvt_pkrtz_f16_f32 v70, v50, v51
	v_cvt_pkrtz_f16_f32 v71, v52, v53
	ds_read_b128 v[2:5], v125 offset:55296
	v_add_f32_e64 v46, v76, -v14
	v_add_f32_e64 v47, v77, -v14
	s_waitcnt lgkmcnt(1)
	v_mfma_f32_32x32x16_f16 v[18:33], v[10:13], v[68:71], v[18:33]
	v_add_f32_e64 v56, v58, -v14
	v_add_f32_e64 v57, v59, -v14
	v_cvt_pkrtz_f16_f32 v72, v46, v47
	v_cvt_pkrtz_f16_f32 v73, v48, v49
	v_cvt_pkrtz_f16_f32 v74, v54, v55
	v_cvt_pkrtz_f16_f32 v75, v56, v57
	ds_read_b128 v[10:13], v125 offset:56320
	v_add_f32_e64 v58, v66, -v14
	v_add_f32_e64 v59, v67, -v14
	s_waitcnt lgkmcnt(1)
	v_mfma_f32_32x32x16_f16 v[18:33], v[2:5], v[72:75], v[18:33]
	ds_read_b128 v[2:5], v125 offset:57344
	ds_read_b128 v[80:83], v125 offset:58368
	v_add_f32_e64 v60, v60, -v14
	v_add_f32_e64 v61, v61, -v14
	v_add_f32_e64 v62, v62, -v14
	v_add_f32_e64 v63, v63, -v14
	v_pk_add_f32 v[64:65], v[64:65], v[14:15] op_sel_hi:[1,0] neg_lo:[0,1] neg_hi:[0,1]
	v_cvt_pkrtz_f16_f32 v76, v58, v59
	v_cvt_pkrtz_f16_f32 v77, v60, v61
	v_cvt_pkrtz_f16_f32 v78, v62, v63
	v_cvt_pkrtz_f16_f32 v79, v64, v65
	s_waitcnt lgkmcnt(2)
	s_nop 0
	v_mfma_f32_32x32x16_f16 v[18:33], v[10:13], v[76:79], v[18:33]
	s_waitcnt lgkmcnt(1)
	v_mfma_f32_32x32x16_f16 v[2:17], v[2:5], v[6:9], 0
	s_waitcnt lgkmcnt(0)
	v_mfma_f32_32x32x16_f16 v[2:17], v[80:83], v[68:71], v[2:17]
	ds_read_b128 v[66:69], v125 offset:59392
	ds_read_b128 v[80:83], v125 offset:60416
	v_lshl_add_u64 v[70:71], v[118:119], 2, s[6:7]
	v_lshl_add_u64 v[70:71], v[70:71], 0, v[90:91]
	global_store_dwordx4 v[70:71], v[42:45], off nt
	global_store_dwordx4 v[70:71], v[38:41], off offset:32 nt
	global_store_dwordx4 v[70:71], v[34:37], off offset:64 nt
	global_store_dwordx4 v[70:71], v[50:53], off offset:96 nt
	global_store_dwordx4 v[70:71], v[46:49], off offset:128 nt
	global_store_dwordx4 v[70:71], v[54:57], off offset:160 nt
	global_store_dwordx4 v[70:71], v[58:61], off offset:192 nt
	global_store_dwordx4 v[70:71], v[62:65], off offset:224 nt
	s_waitcnt lgkmcnt(1)
	v_mfma_f32_32x32x16_f16 v[2:17], v[66:69], v[72:75], v[2:17]
	s_waitcnt lgkmcnt(0)
	v_mfma_f32_32x32x16_f16 v[2:17], v[80:83], v[76:79], v[2:17]
	ds_read_b128 v[66:69], v92 offset:62784
	ds_read_b128 v[70:73], v92 offset:63040
	ds_read_b128 v[74:77], v92 offset:63296
	ds_read_b128 v[78:81], v92 offset:63552
	ds_read_b128 v[82:85], v92 offset:62816
	s_waitcnt lgkmcnt(4)
	v_add_f32_e32 v18, v66, v18
	v_mul_f32_e32 v18, 0x3f7fffac, v18
	v_add_f32_e32 v19, v67, v19
	s_waitcnt lgkmcnt(2)
	v_fma_f32 v18, v70, v18, v74
	v_mul_f32_e32 v19, 0x3f7fffac, v19
	v_max_f32_e32 v18, 0, v18
	v_fma_f32 v19, v71, v19, v75
	s_waitcnt lgkmcnt(1)
	v_fma_f32 v18, v78, v18, 0
	v_max_f32_e32 v19, 0, v19
	v_fmac_f32_e32 v18, v79, v19
	v_add_f32_e32 v19, v68, v20
	v_mul_f32_e32 v19, 0x3f7fffac, v19
	v_fma_f32 v19, v72, v19, v76
	v_max_f32_e32 v19, 0, v19
	v_fmac_f32_e32 v18, v80, v19
	v_add_f32_e32 v19, v69, v21
	ds_read_b128 v[86:89], v92 offset:63072
	ds_read_b128 v[94:97], v92 offset:63328
	v_mul_f32_e32 v19, 0x3f7fffac, v19
	v_fmac_f32_e32 v77, v73, v19
	ds_read_b128 v[98:101], v92 offset:63584
	v_max_f32_e32 v19, 0, v77
	v_fmac_f32_e32 v18, v81, v19
	s_waitcnt lgkmcnt(3)
	v_add_f32_e32 v19, v82, v22
	v_mul_f32_e32 v19, 0x3f7fffac, v19
	s_waitcnt lgkmcnt(1)
	v_fma_f32 v19, v86, v19, v94
	v_max_f32_e32 v19, 0, v19
	s_waitcnt lgkmcnt(0)
	v_fmac_f32_e32 v18, v98, v19
	v_add_f32_e32 v19, v83, v23
	v_mul_f32_e32 v19, 0x3f7fffac, v19
	v_fma_f32 v19, v87, v19, v95
	v_max_f32_e32 v19, 0, v19
	v_fmac_f32_e32 v18, v99, v19
	v_add_f32_e32 v19, v84, v24
	v_mul_f32_e32 v19, 0x3f7fffac, v19
	v_fma_f32 v19, v88, v19, v96
	v_max_f32_e32 v19, 0, v19
	v_fmac_f32_e32 v18, v100, v19
	v_add_f32_e32 v19, v85, v25
	v_mul_f32_e32 v19, 0x3f7fffac, v19
	v_fmac_f32_e32 v97, v89, v19
	v_max_f32_e32 v19, 0, v97
	ds_read_b128 v[20:23], v92 offset:62848
	ds_read_b128 v[66:69], v92 offset:63104
	ds_read_b128 v[70:73], v92 offset:63360
	ds_read_b128 v[74:77], v92 offset:63616
	ds_read_b128 v[78:81], v92 offset:62880
	v_fmac_f32_e32 v18, v101, v19
	s_waitcnt lgkmcnt(4)
	v_add_f32_e32 v19, v20, v26
	v_mul_f32_e32 v19, 0x3f7fffac, v19
	s_waitcnt lgkmcnt(2)
	v_fma_f32 v19, v66, v19, v70
	v_max_f32_e32 v19, 0, v19
	s_waitcnt lgkmcnt(1)
	v_fmac_f32_e32 v18, v74, v19
	v_add_f32_e32 v19, v21, v27
	v_mul_f32_e32 v19, 0x3f7fffac, v19
	v_fma_f32 v19, v67, v19, v71
	v_max_f32_e32 v19, 0, v19
	v_fmac_f32_e32 v18, v75, v19
	v_add_f32_e32 v19, v22, v28
	v_mul_f32_e32 v19, 0x3f7fffac, v19
	v_fma_f32 v19, v68, v19, v72
	v_max_f32_e32 v19, 0, v19
	v_fmac_f32_e32 v18, v76, v19
	v_add_f32_e32 v19, v23, v29
	ds_read_b128 v[82:85], v92 offset:63136
	ds_read_b128 v[86:89], v92 offset:63392
	v_mul_f32_e32 v19, 0x3f7fffac, v19
	v_fmac_f32_e32 v73, v69, v19
	ds_read_b128 v[94:97], v92 offset:63648
	v_max_f32_e32 v19, 0, v73
	v_fmac_f32_e32 v18, v77, v19
	s_waitcnt lgkmcnt(3)
	v_add_f32_e32 v19, v78, v30
	v_mul_f32_e32 v19, 0x3f7fffac, v19
	s_waitcnt lgkmcnt(1)
	v_fma_f32 v19, v82, v19, v86
	v_max_f32_e32 v19, 0, v19
	s_waitcnt lgkmcnt(0)
	v_fmac_f32_e32 v18, v94, v19
	v_add_f32_e32 v19, v79, v31
	v_mul_f32_e32 v19, 0x3f7fffac, v19
	v_fma_f32 v19, v83, v19, v87
	v_max_f32_e32 v19, 0, v19
	v_fmac_f32_e32 v18, v95, v19
	v_add_f32_e32 v19, v80, v32
	v_mul_f32_e32 v19, 0x3f7fffac, v19
	v_fma_f32 v19, v84, v19, v88
	v_max_f32_e32 v19, 0, v19
	v_fmac_f32_e32 v18, v96, v19
	v_add_f32_e32 v19, v81, v33
	ds_read_b128 v[20:23], v92 offset:62912
	ds_read_b128 v[24:27], v92 offset:63168
	ds_read_b128 v[28:31], v92 offset:63424
	ds_read_b128 v[66:69], v92 offset:63680
	ds_read_b128 v[70:73], v92 offset:62944
	v_mul_f32_e32 v19, 0x3f7fffac, v19
	s_waitcnt lgkmcnt(4)
	v_add_f32_e32 v2, v20, v2
	v_fmac_f32_e32 v89, v85, v19
	v_mul_f32_e32 v2, 0x3f7fffac, v2
	v_max_f32_e32 v19, 0, v89
	s_waitcnt lgkmcnt(2)
	v_fma_f32 v2, v24, v2, v28
	v_fmac_f32_e32 v18, v97, v19
	v_max_f32_e32 v2, 0, v2
	s_waitcnt lgkmcnt(1)
	v_fmac_f32_e32 v18, v66, v2
	v_add_f32_e32 v2, v21, v3
	v_mul_f32_e32 v2, 0x3f7fffac, v2
	v_fma_f32 v2, v25, v2, v29
	v_max_f32_e32 v2, 0, v2
	v_fmac_f32_e32 v18, v67, v2
	v_add_f32_e32 v2, v22, v4
	v_mul_f32_e32 v2, 0x3f7fffac, v2
	v_fma_f32 v2, v26, v2, v30
	v_max_f32_e32 v2, 0, v2
	v_fmac_f32_e32 v18, v68, v2
	v_add_f32_e32 v2, v23, v5
	ds_read_b128 v[74:77], v92 offset:63200
	ds_read_b128 v[78:81], v92 offset:63456
	v_mul_f32_e32 v2, 0x3f7fffac, v2
	v_fmac_f32_e32 v31, v27, v2
	ds_read_b128 v[82:85], v92 offset:63712
	v_max_f32_e32 v2, 0, v31
	v_fmac_f32_e32 v18, v69, v2
	s_waitcnt lgkmcnt(3)
	v_add_f32_e32 v2, v70, v6
	v_mul_f32_e32 v2, 0x3f7fffac, v2
	s_waitcnt lgkmcnt(1)
	v_fma_f32 v2, v74, v2, v78
	v_max_f32_e32 v2, 0, v2
	s_waitcnt lgkmcnt(0)
	v_fmac_f32_e32 v18, v82, v2
	v_add_f32_e32 v2, v71, v7
	v_mul_f32_e32 v2, 0x3f7fffac, v2
	v_fma_f32 v2, v75, v2, v79
	v_max_f32_e32 v2, 0, v2
	v_fmac_f32_e32 v18, v83, v2
	v_add_f32_e32 v2, v72, v8
	v_mul_f32_e32 v2, 0x3f7fffac, v2
	v_fma_f32 v2, v76, v2, v80
	v_max_f32_e32 v2, 0, v2
	v_fmac_f32_e32 v18, v84, v2
	v_add_f32_e32 v2, v73, v9
	v_mul_f32_e32 v2, 0x3f7fffac, v2
	v_fmac_f32_e32 v81, v77, v2
	v_max_f32_e32 v2, 0, v81
	v_fmac_f32_e32 v18, v85, v2
	ds_read_b128 v[2:5], v92 offset:62976
	ds_read_b128 v[6:9], v92 offset:63232
	ds_read_b128 v[20:23], v92 offset:63488
	ds_read_b128 v[24:27], v92 offset:63744
	ds_read_b128 v[28:31], v92 offset:63008
	s_waitcnt lgkmcnt(4)
	v_add_f32_e32 v2, v2, v10
	v_mul_f32_e32 v2, 0x3f7fffac, v2
	s_waitcnt lgkmcnt(2)
	v_fma_f32 v2, v6, v2, v20
	v_max_f32_e32 v2, 0, v2
	s_waitcnt lgkmcnt(1)
	v_fmac_f32_e32 v18, v24, v2
	v_add_f32_e32 v2, v3, v11
	v_mul_f32_e32 v2, 0x3f7fffac, v2
	v_fma_f32 v2, v7, v2, v21
	v_max_f32_e32 v2, 0, v2
	v_fmac_f32_e32 v18, v25, v2
	v_add_f32_e32 v2, v4, v12
	v_mul_f32_e32 v2, 0x3f7fffac, v2
	v_fma_f32 v2, v8, v2, v22
	v_max_f32_e32 v2, 0, v2
	v_fmac_f32_e32 v18, v26, v2
	v_add_f32_e32 v2, v5, v13
	ds_read_b128 v[66:69], v92 offset:63264
	ds_read_b128 v[70:73], v92 offset:63520
	v_mul_f32_e32 v2, 0x3f7fffac, v2
	v_fmac_f32_e32 v23, v9, v2
	ds_read_b128 v[74:77], v92 offset:63776
	v_max_f32_e32 v2, 0, v23
	v_fmac_f32_e32 v18, v27, v2
	s_waitcnt lgkmcnt(3)
	v_add_f32_e32 v2, v28, v14
	v_mul_f32_e32 v2, 0x3f7fffac, v2
	s_waitcnt lgkmcnt(1)
	v_fma_f32 v2, v66, v2, v70
	v_max_f32_e32 v2, 0, v2
	s_waitcnt lgkmcnt(0)
	v_fmac_f32_e32 v18, v74, v2
	v_add_f32_e32 v2, v29, v15
	v_mul_f32_e32 v2, 0x3f7fffac, v2
	v_fma_f32 v2, v67, v2, v71
	v_max_f32_e32 v2, 0, v2
	v_fmac_f32_e32 v18, v75, v2
	v_add_f32_e32 v2, v30, v16
	v_mul_f32_e32 v2, 0x3f7fffac, v2
	v_fma_f32 v2, v68, v2, v72
	v_max_f32_e32 v2, 0, v2
	v_fmac_f32_e32 v18, v76, v2
	v_add_f32_e32 v2, v31, v17
	v_mul_f32_e32 v2, 0x3f7fffac, v2
	v_fmac_f32_e32 v73, v69, v2
	v_max_f32_e32 v2, 0, v73
	v_fmac_f32_e32 v18, v77, v2
	v_mov_b32_e32 v2, v18
	v_mov_b32_e32 v3, v18
	s_nop 1
	v_permlane32_swap_b32_e32 v2, v3
	s_and_saveexec_b64 s[4:5], s[0:1]
	s_cbranch_execz .LBB2_99
	v_lshl_or_b32 v4, s12, 7, v1
	v_ashrrev_i32_e32 v5, 31, v4
	v_cndmask_b32_e64 v1, v2, v3, s[2:3]
	v_lshl_add_u64 v[4:5], v[4:5], 2, s[8:9]
	v_add_f32_e32 v1, v18, v1
	global_store_dword v[4:5], v1, off

.LBB4_37:
	v_lshlrev_b32_e32 v76, 4, v44
	v_mov_b32_e32 v77, 0
	v_lshl_add_u64 v[76:77], s[8:9], 0, v[76:77]
	s_mov_b64 s[2:3], 0x41000
	v_lshl_add_u64 v[76:77], v[76:77], 0, s[2:3]
	s_lshl_b32 s6, s34, 10
	s_mov_b32 s7, 0
	s_add_i32 m0, s6, 0x2000
	v_lshl_add_u64 v[78:79], v[76:77], 0, s[6:7]
	global_load_lds_dwordx4 v[78:79], off
	s_addk_i32 s6, 0x3000
	s_add_i32 m0, s6, 0x2000
	v_lshl_add_u64 v[78:79], v[76:77], 0, s[6:7]
	global_load_lds_dwordx4 v[78:79], off
	s_addk_i32 s6, 0x3000
	s_add_i32 m0, s6, 0x2000
	v_lshl_add_u64 v[78:79], v[76:77], 0, s[6:7]
	global_load_lds_dwordx4 v[78:79], off
	s_addk_i32 s6, 0x3000
	s_add_i32 m0, s6, 0x2000
	v_lshl_add_u64 v[78:79], v[76:77], 0, s[6:7]
	global_load_lds_dwordx4 v[78:79], off
	s_addk_i32 s6, 0x3000
	s_add_i32 m0, s6, 0x2000
	v_lshl_add_u64 v[78:79], v[76:77], 0, s[6:7]
	global_load_lds_dwordx4 v[78:79], off
	s_addk_i32 s6, 0x3000
	s_add_i32 m0, s6, 0x2000
	v_lshl_add_u64 v[78:79], v[76:77], 0, s[6:7]
	global_load_lds_dwordx4 v[78:79], off
	v_lshl_add_u32 v6, v0, 1, 0
	v_add_u32_e32 v6, 0x21c80, v6
	s_waitcnt vmcnt(6)
	ds_write_b16 v6, v9
	ds_write_b16 v6, v10 offset:1536
	v_lshl_add_u32 v6, v0, 2, 0
	s_and_saveexec_b64 s[2:3], vcc
	v_add_u32_e32 v7, 0x22880, v6
	ds_write_b32 v7, v11
	s_or_b64 exec, exec, s[2:3]
	s_movk_i32 s2, 0x1c0
	v_cmp_gt_u32_e32 vcc, s2, v0
	s_and_saveexec_b64 s[2:3], vcc
	v_add_u32_e32 v6, 0x22c80, v6
	ds_write_b32 v6, v12
	s_or_b64 exec, exec, s[2:3]
	s_movk_i32 s2, 0x200
	v_cmp_gt_u32_e32 vcc, s2, v0
	s_and_saveexec_b64 s[2:3], vcc
	s_cbranch_execz .LBB4_43
	v_bfe_i32 v7, v0, 6, 1
	v_lshrrev_b32_e32 v6, 7, v0
	v_and_b32_e32 v7, 0x61, v7
	s_movk_i32 s6, 0x62
	v_mad_u32_u24 v6, v6, s6, v7
	v_mul_u32_u24_e32 v6, 0x90, v6
	s_add_i32 s6, 0, 0x14000
	v_lshlrev_b32_e32 v7, 1, v44
	v_add3_u32 v6, s6, v6, v7
	v_mov_b32_e32 v7, 0
	ds_write_b16 v6, v7
.LBB4_43:
	s_or_b64 exec, exec, s[2:3]
	v_lshlrev_b32_e32 v42, 4, v44
	v_mov_b32_e32 v43, 0
	s_waitcnt vmcnt(6)
	s_waitcnt lgkmcnt(0)
	s_barrier
	s_load_dwordx4 s[8:11], s[0:1], 0x88
	s_andn2_b64 vcc, exec, s[4:5]
	v_mbcnt_lo_u32_b32 v43, -1, 0
	s_cbranch_vccnz .LBB4_47
	v_mbcnt_hi_u32_b32 v7, -1, v43
	v_and_b32_e32 v6, 64, v7
	v_add_u32_e32 v10, 64, v6
	v_xor_b32_e32 v6, 1, v7
	v_cmp_lt_i32_e32 vcc, v6, v10
	v_xor_b32_e32 v9, 2, v7
	v_xor_b32_e32 v16, 32, v7
	v_cndmask_b32_e32 v6, v7, v6, vcc
	v_lshlrev_b32_e32 v11, 2, v6
	ds_bpermute_b32 v6, v11, v3
	v_cmp_lt_i32_e32 vcc, v9, v10
	v_cvt_f32_i32_e32 v19, v5
	s_mov_b32 s13, 0x800000
	s_mov_b32 s12, 0x3f317217
	s_waitcnt lgkmcnt(0)
	v_add_f32_e32 v3, v3, v6
	v_cndmask_b32_e32 v6, v7, v9, vcc
	v_lshlrev_b32_e32 v12, 2, v6
	ds_bpermute_b32 v6, v12, v3
	v_xor_b32_e32 v9, 4, v7
	v_cmp_lt_i32_e32 vcc, v9, v10
	s_mov_b32 s14, 0x7f800000
	s_waitcnt lgkmcnt(0)
	v_add_f32_e32 v3, v3, v6
	v_cndmask_b32_e32 v6, v7, v9, vcc
	v_lshlrev_b32_e32 v13, 2, v6
	ds_bpermute_b32 v6, v13, v3
	v_xor_b32_e32 v9, 8, v7
	v_cmp_lt_i32_e32 vcc, v9, v10
	s_waitcnt lgkmcnt(0)
	v_add_f32_e32 v3, v3, v6
	v_cndmask_b32_e32 v6, v7, v9, vcc
	v_lshlrev_b32_e32 v14, 2, v6
	ds_bpermute_b32 v6, v14, v3
	v_xor_b32_e32 v9, 16, v7
	v_cmp_lt_i32_e32 vcc, v9, v10
	s_waitcnt lgkmcnt(0)
	v_add_f32_e32 v3, v3, v6
	v_cndmask_b32_e32 v6, v7, v9, vcc
	v_lshlrev_b32_e32 v15, 2, v6
	ds_bpermute_b32 v9, v15, v3
	v_cmp_lt_i32_e32 vcc, v16, v10
	ds_bpermute_b32 v6, v11, v2
	s_waitcnt lgkmcnt(0)
	v_add_f32_e32 v9, v3, v9
	v_lshlrev_b32_e32 v3, 2, v7
	v_and_b32_e32 v3, 0x100, v3
	v_cndmask_b32_e32 v10, v7, v16, vcc
	ds_bpermute_b32 v7, v3, v8
	ds_bpermute_b32 v16, v3, v5
	ds_bpermute_b32 v17, v3, v8 offset:4
	ds_bpermute_b32 v18, v3, v5 offset:4
	ds_bpermute_b32 v20, v3, v8 offset:12
	s_waitcnt lgkmcnt(0)
	v_cmp_eq_u32_e32 vcc, v7, v44
	ds_bpermute_b32 v21, v3, v5 offset:12
	ds_bpermute_b32 v22, v3, v5 offset:20
	v_cndmask_b32_e32 v7, 0, v16, vcc
	v_cmp_eq_u32_e32 vcc, v17, v44
	ds_bpermute_b32 v17, v3, v8 offset:8
	s_nop 0
	v_cndmask_b32_e32 v16, 0, v18, vcc
	ds_bpermute_b32 v18, v3, v5 offset:8
	v_add_u32_e32 v7, v16, v7
	s_waitcnt lgkmcnt(0)
	v_cmp_eq_u32_e32 vcc, v17, v44
	s_nop 1
	v_cndmask_b32_e32 v16, 0, v18, vcc
	ds_bpermute_b32 v18, v3, v8 offset:16
	v_cmp_eq_u32_e32 vcc, v20, v44
	ds_bpermute_b32 v20, v3, v5 offset:16
	s_nop 0
	v_cndmask_b32_e32 v17, 0, v21, vcc
	ds_bpermute_b32 v21, v3, v8 offset:20
	s_waitcnt lgkmcnt(0)
	v_cmp_eq_u32_e32 vcc, v18, v44
	ds_bpermute_b32 v18, v3, v8 offset:24
	v_add3_u32 v7, v7, v16, v17
	v_cndmask_b32_e32 v16, 0, v20, vcc
	ds_bpermute_b32 v20, v3, v5 offset:24
	v_cmp_eq_u32_e32 vcc, v21, v44
	ds_bpermute_b32 v21, v3, v8 offset:28
	s_nop 0
	v_cndmask_b32_e32 v17, 0, v22, vcc
	ds_bpermute_b32 v22, v3, v5 offset:28
	s_waitcnt lgkmcnt(0)
	v_cmp_eq_u32_e32 vcc, v18, v44
	ds_bpermute_b32 v18, v3, v8 offset:32
	v_add3_u32 v7, v7, v16, v17
	v_cndmask_b32_e32 v16, 0, v20, vcc
	ds_bpermute_b32 v20, v3, v5 offset:32
	v_cmp_eq_u32_e32 vcc, v21, v44
	ds_bpermute_b32 v21, v3, v8 offset:36
	s_nop 0
	v_cndmask_b32_e32 v17, 0, v22, vcc
	ds_bpermute_b32 v22, v3, v5 offset:36
	s_waitcnt lgkmcnt(0)
	v_cmp_eq_u32_e32 vcc, v18, v44
	ds_bpermute_b32 v18, v3, v8 offset:40
	v_add3_u32 v7, v7, v16, v17
	v_cndmask_b32_e32 v16, 0, v20, vcc
	ds_bpermute_b32 v20, v3, v5 offset:40
	v_cmp_eq_u32_e32 vcc, v21, v44
	ds_bpermute_b32 v21, v3, v8 offset:44
	s_nop 0
	v_cndmask_b32_e32 v17, 0, v22, vcc
	ds_bpermute_b32 v22, v3, v5 offset:44
	s_waitcnt lgkmcnt(0)
	v_cmp_eq_u32_e32 vcc, v18, v44
	ds_bpermute_b32 v18, v3, v8 offset:48
	v_add3_u32 v7, v7, v16, v17
	v_cndmask_b32_e32 v16, 0, v20, vcc
	ds_bpermute_b32 v20, v3, v5 offset:48
	v_cmp_eq_u32_e32 vcc, v21, v44
	ds_bpermute_b32 v21, v3, v8 offset:52
	s_nop 0
	v_cndmask_b32_e32 v17, 0, v22, vcc
	ds_bpermute_b32 v22, v3, v5 offset:52
	s_waitcnt lgkmcnt(0)
	v_cmp_eq_u32_e32 vcc, v18, v44
	ds_bpermute_b32 v18, v3, v8 offset:56
	v_add3_u32 v7, v7, v16, v17
	v_cndmask_b32_e32 v16, 0, v20, vcc
	ds_bpermute_b32 v20, v3, v5 offset:56
	ds_bpermute_b32 v8, v3, v8 offset:60
	ds_bpermute_b32 v3, v3, v5 offset:60
	v_cmp_eq_u32_e32 vcc, v21, v44
	s_nop 1
	v_cndmask_b32_e32 v17, 0, v22, vcc
	s_waitcnt lgkmcnt(0)
	v_cmp_eq_u32_e32 vcc, v18, v44
	v_add3_u32 v5, v7, v16, v17
	v_mul_f32_e32 v17, 0x39000000, v19
	v_cndmask_b32_e32 v7, 0, v20, vcc
	v_cmp_eq_u32_e32 vcc, v8, v44
	s_nop 1
	v_cndmask_b32_e32 v3, 0, v3, vcc
	v_add3_u32 v5, v5, v7, v3
	v_mul_f32_e32 v3, v4, v19
	v_cvt_f32_i32_e32 v4, v5
	v_mov_b32_e32 v5, 0x2edbe6ff
	v_fmamk_f32 v7, v19, 0x39000000, v5
	v_cmp_gt_f32_e32 vcc, s13, v7
	v_fmac_f32_e32 v5, 0x39000000, v4
	v_mul_f32_e32 v16, 0x39000000, v4
	v_cndmask_b32_e64 v8, 0, 32, vcc
	v_ldexp_f32 v7, v7, v8
	v_log_f32_e32 v7, v7
	s_nop 0
	v_mul_f32_e32 v8, 0x3f317217, v7
	v_fma_f32 v8, v7, s12, -v8
	v_fmac_f32_e32 v8, 0x3377d1cf, v7
	v_fmac_f32_e32 v8, 0x3f317217, v7
	v_cmp_lt_f32_e64 s[2:3], |v7|, s14
	s_nop 1
	v_cndmask_b32_e64 v7, v7, v8, s[2:3]
	v_mov_b32_e32 v8, 0x41b17218
	v_cndmask_b32_e32 v18, 0, v8, vcc
	v_cmp_gt_f32_e32 vcc, s13, v5
	v_sub_f32_e32 v7, v7, v18
	v_cmp_gt_u32_e64 s[2:3], 16, v44
	v_cndmask_b32_e64 v4, 0, 32, vcc
	v_ldexp_f32 v4, v5, v4
	v_log_f32_e32 v4, v4
	v_mul_f32_e32 v5, v17, v7
	v_cndmask_b32_e64 v5, 0, v5, s[2:3]
	ds_bpermute_b32 v17, v11, v5
	v_mul_f32_e32 v7, 0x3f317217, v4
	v_fma_f32 v7, v4, s12, -v7
	v_fmac_f32_e32 v7, 0x3377d1cf, v4
	v_fmac_f32_e32 v7, 0x3f317217, v4
	v_cmp_lt_f32_e64 s[4:5], |v4|, s14
	s_waitcnt lgkmcnt(0)
	v_add_f32_e32 v17, v5, v17
	ds_bpermute_b32 v18, v12, v17
	v_cndmask_b32_e64 v4, v4, v7, s[4:5]
	v_cndmask_b32_e32 v7, 0, v8, vcc
	v_sub_f32_e32 v4, v4, v7
	v_mul_f32_e32 v4, v16, v4
	v_cndmask_b32_e64 v16, 0, v4, s[2:3]
	ds_bpermute_b32 v7, v11, v3
	ds_bpermute_b32 v11, v11, v16
	v_cmp_eq_u32_e32 vcc, 0, v44
	s_waitcnt lgkmcnt(0)
	v_pk_add_f32 v[2:3], v[2:3], v[6:7]
	v_add_f32_e32 v6, v16, v11
	ds_bpermute_b32 v4, v12, v2
	ds_bpermute_b32 v5, v12, v3
	ds_bpermute_b32 v11, v12, v6
	v_add_f32_e32 v7, v17, v18
	ds_bpermute_b32 v12, v13, v7
	s_waitcnt lgkmcnt(0)
	v_pk_add_f32 v[2:3], v[2:3], v[4:5]
	v_add_f32_e32 v6, v6, v11
	ds_bpermute_b32 v4, v13, v2
	ds_bpermute_b32 v5, v13, v3
	ds_bpermute_b32 v11, v13, v6
	v_add_f32_e32 v7, v7, v12
	ds_bpermute_b32 v12, v14, v7
	v_lshlrev_b32_e32 v13, 2, v10
	s_waitcnt lgkmcnt(0)
	v_pk_add_f32 v[2:3], v[2:3], v[4:5]
	v_add_f32_e32 v6, v6, v11
	ds_bpermute_b32 v4, v14, v2
	ds_bpermute_b32 v5, v14, v3
	ds_bpermute_b32 v10, v14, v6
	v_add_f32_e32 v7, v7, v12
	ds_bpermute_b32 v11, v15, v7
	s_waitcnt lgkmcnt(0)
	v_pk_add_f32 v[2:3], v[2:3], v[4:5]
	v_add_f32_e32 v10, v6, v10
	ds_bpermute_b32 v4, v15, v2
	ds_bpermute_b32 v5, v15, v3
	ds_bpermute_b32 v12, v15, v10
	v_add_f32_e32 v7, v7, v11
	ds_bpermute_b32 v6, v13, v9
	ds_bpermute_b32 v11, v13, v7
	s_waitcnt lgkmcnt(0)
	v_pk_add_f32 v[2:3], v[2:3], v[4:5]
	v_add_f32_e32 v10, v10, v12
	ds_bpermute_b32 v4, v13, v2
	ds_bpermute_b32 v5, v13, v3
	ds_bpermute_b32 v12, v13, v10
	s_and_saveexec_b64 s[6:7], vcc
	s_cbranch_execz .LBB4_46
	v_add_f32_e32 v7, v7, v11
	s_waitcnt lgkmcnt(0)
	v_pk_add_f32 v[2:3], v[2:3], v[4:5]
	s_mov_b32 s2, 0xbfb8aa3b
	v_mul_f32_e32 v5, 0xbfb8aa3b, v7
	v_add_f32_e32 v4, v9, v6
	v_fma_f32 v6, v7, s2, -v5
	v_rndne_f32_e32 v9, v5
	v_fmac_f32_e32 v6, 0xb2a5705f, v7
	v_sub_f32_e32 v5, v5, v9
	v_add_f32_e32 v5, v5, v6
	v_exp_f32_e32 v5, v5
	v_cvt_i32_f32_e32 v6, v9
	v_add_f32_e32 v10, v10, v12
	v_add_f32_e32 v2, v2, v3
	s_mov_b32 s3, 0x42ce8ed0
	v_ldexp_f32 v3, v5, v6
	v_mul_f32_e32 v5, 0xbfb8aa3b, v10
	v_fma_f32 v6, v10, s2, -v5
	v_rndne_f32_e32 v9, v5
	v_fmac_f32_e32 v6, 0xb2a5705f, v10
	v_sub_f32_e32 v5, v5, v9
	v_cmp_nlt_f32_e32 vcc, s3, v7
	s_mov_b32 s4, 0xc2b17218
	v_add_f32_e32 v5, v5, v6
	v_cndmask_b32_e32 v3, 0, v3, vcc
	v_exp_f32_e32 v5, v5
	v_cvt_i32_f32_e32 v6, v9
	v_mov_b32_e32 v9, 0x7f800000
	v_cmp_ngt_f32_e32 vcc, s4, v7
	v_cmp_nlt_f32_e64 s[2:3], s3, v10
	v_ldexp_f32 v5, v5, v6
	v_cndmask_b32_e32 v3, v9, v3, vcc
	v_add_f32_e32 v3, 0x2edbe6ff, v3
	v_cmp_gt_f32_e32 vcc, s13, v3
	v_cndmask_b32_e64 v5, 0, v5, s[2:3]
	v_cmp_ngt_f32_e64 s[2:3], s4, v10
	v_cndmask_b32_e64 v6, 0, 32, vcc
	v_ldexp_f32 v3, v3, v6
	v_log_f32_e32 v3, v3
	v_cndmask_b32_e64 v5, v9, v5, s[2:3]
	v_add_f32_e32 v5, 0x2edbe6ff, v5
	v_cmp_gt_f32_e64 s[2:3], s13, v5
	v_mul_f32_e32 v6, 0x3f317217, v3
	v_fma_f32 v6, v3, s12, -v6
	v_cndmask_b32_e64 v7, 0, 32, s[2:3]
	v_ldexp_f32 v5, v5, v7
	v_log_f32_e32 v5, v5
	v_fmac_f32_e32 v6, 0x3377d1cf, v3
	v_fmac_f32_e32 v6, 0x3f317217, v3
	v_cmp_lt_f32_e64 s[4:5], |v3|, s14
	v_mul_f32_e32 v2, 0x3fa00000, v2
	v_mul_f32_e32 v2, 0x34aaaaab, v2
	v_cndmask_b32_e64 v3, v3, v6, s[4:5]
	v_cndmask_b32_e32 v6, 0, v8, vcc
	v_sub_f32_e32 v3, v3, v6
	v_mul_f32_e32 v6, 0x3f317217, v5
	v_fma_f32 v6, v5, s12, -v6
	v_fmac_f32_e32 v6, 0x3377d1cf, v5
	v_fmac_f32_e32 v6, 0x3f317217, v5
	v_cmp_lt_f32_e64 vcc, |v5|, s14
	s_mov_b32 s4, 0x4a400000
	s_nop 0
	v_cndmask_b32_e32 v5, v5, v6, vcc
	v_cndmask_b32_e64 v6, 0, v8, s[2:3]
	v_div_scale_f32 v7, s[2:3], s4, s4, v4
	v_rcp_f32_e32 v8, v7
	v_sub_f32_e32 v5, v5, v6
	v_add_f32_e32 v3, v3, v5
	v_mul_f32_e32 v3, 0xbdcccccd, v3
	v_fma_f32 v5, -v7, v8, 1.0
	v_fmac_f32_e32 v8, v5, v8
	v_div_scale_f32 v5, vcc, v4, s4, v4
	v_mul_f32_e32 v6, v5, v8
	v_fma_f32 v9, -v7, v6, v5
	v_fmac_f32_e32 v6, v9, v8
	v_fma_f32 v5, -v7, v6, v5
	v_div_fmas_f32 v5, v5, v8, v6
	v_div_fixup_f32 v4, v5, s4, v4
	v_mov_b32_e32 v5, 0
	global_store_dword v5, v2, s[10:11] sc1
	global_store_dword v5, v3, s[10:11] offset:4 sc1
	global_store_dword v5, v4, s[10:11] offset:8 sc1

	.amdhsa_kernel _Z7k5_convPKDF16_PKiS0_PKfS4_S4_S4_S4_S4_S4_S4_PfS4_S4_S2_S2_S4_PiS5_S5_
		.amdhsa_group_segment_fixed_size 0
		.amdhsa_private_segment_fixed_size 0
		.amdhsa_kernarg_size 416
		.amdhsa_user_sgpr_count 2
		.amdhsa_user_sgpr_dispatch_ptr 0
		.amdhsa_user_sgpr_queue_ptr 0
		.amdhsa_user_sgpr_kernarg_segment_ptr 1
		.amdhsa_user_sgpr_dispatch_id 0
		.amdhsa_user_sgpr_kernarg_preload_length 0
		.amdhsa_user_sgpr_kernarg_preload_offset 0
		.amdhsa_user_sgpr_private_segment_size 0
		.amdhsa_uses_dynamic_stack 0
		.amdhsa_enable_private_segment 0
		.amdhsa_system_sgpr_workgroup_id_x 1
		.amdhsa_system_sgpr_workgroup_id_y 0
		.amdhsa_system_sgpr_workgroup_id_z 0
		.amdhsa_system_sgpr_workgroup_info 0
		.amdhsa_system_vgpr_workitem_id 0
		.amdhsa_next_free_vgpr 80
		.amdhsa_next_free_sgpr 45
		.amdhsa_accum_offset 80
		.amdhsa_reserve_vcc 1
		.amdhsa_float_round_mode_32 0
		.amdhsa_float_round_mode_16_64 0
		.amdhsa_float_denorm_mode_32 3
		.amdhsa_float_denorm_mode_16_64 3
		.amdhsa_dx10_clamp 1
		.amdhsa_ieee_mode 1
		.amdhsa_fp16_overflow 0
		.amdhsa_tg_split 0
		.amdhsa_exception_fp_ieee_invalid_op 0
		.amdhsa_exception_fp_denorm_src 0
		.amdhsa_exception_fp_ieee_div_zero 0
		.amdhsa_exception_fp_ieee_overflow 0
		.amdhsa_exception_fp_ieee_underflow 0
		.amdhsa_exception_fp_ieee_inexact 0
		.amdhsa_exception_int_div_zero 0
	.end_amdhsa_kernel

amdhsa.kernels:
  - .agpr_count:     0
    .args:
      - .offset:         0
        .size:           272
        .value_kind:     by_value
    .group_segment_fixed_size: 27780
    .kernarg_segment_align: 8
    .kernarg_segment_size: 272
    .language:       OpenCL C
    .language_version:
      - 2
      - 0
    .max_flat_workgroup_size: 1024
    .name:           _Z6k_prep5PrepP
    .private_segment_fixed_size: 0
    .sgpr_count:     106
    .sgpr_spill_count: 0
    .symbol:         _Z6k_prep5PrepP.kd
    .uniform_work_group_size: 1
    .uses_dynamic_stack: false
    .vgpr_count:     67
    .vgpr_spill_count: 0
    .wavefront_size: 64
  - .agpr_count:     0
    .args:
      - .actual_access:  read_only
        .address_space:  global
        .offset:         0
        .size:           8
        .value_kind:     global_buffer
      - .actual_access:  read_only
        .address_space:  global
        .offset:         8
        .size:           8
        .value_kind:     global_buffer
      - .actual_access:  read_only
        .address_space:  global
        .offset:         16
        .size:           8
        .value_kind:     global_buffer
      - .address_space:  global
        .offset:         24
        .size:           8
        .value_kind:     global_buffer
      - .actual_access:  read_only
        .address_space:  global
        .offset:         32
        .size:           8
        .value_kind:     global_buffer
      - .actual_access:  read_only
        .address_space:  global
        .offset:         40
        .size:           8
        .value_kind:     global_buffer
      - .actual_access:  read_only
        .address_space:  global
        .offset:         48
        .size:           8
        .value_kind:     global_buffer
      - .actual_access:  read_only
        .address_space:  global
        .offset:         56
        .size:           8
        .value_kind:     global_buffer
      - .actual_access:  write_only
        .address_space:  global
        .offset:         64
        .size:           8
        .value_kind:     global_buffer
    .group_segment_fixed_size: 0
    .kernarg_segment_align: 8
    .kernarg_segment_size: 72
    .language:       OpenCL C
    .language_version:
      - 2
      - 0
    .max_flat_workgroup_size: 384
    .name:           _Z11k1_temporalPKfS0_S0_PKDF16_S0_S0_S0_S0_Pf
    .private_segment_fixed_size: 0
    .sgpr_count:     34
    .sgpr_spill_count: 0
    .symbol:         _Z11k1_temporalPKfS0_S0_PKDF16_S0_S0_S0_S0_Pf.kd
    .uniform_work_group_size: 1
    .uses_dynamic_stack: false
    .vgpr_count:     247
    .vgpr_spill_count: 0
    .wavefront_size: 64
  - .agpr_count:     0
    .args:
      - .address_space:  global
        .offset:         0
        .size:           8
        .value_kind:     global_buffer
      - .address_space:  global
        .offset:         8
        .size:           8
        .value_kind:     global_buffer
      - .actual_access:  read_only
        .address_space:  global
        .offset:         16
        .size:           8
        .value_kind:     global_buffer
      - .actual_access:  read_only
        .address_space:  global
        .offset:         24
        .size:           8
        .value_kind:     global_buffer
      - .actual_access:  read_only
        .address_space:  global
        .offset:         32
        .size:           8
        .value_kind:     global_buffer
      - .actual_access:  read_only
        .address_space:  global
        .offset:         40
        .size:           8
        .value_kind:     global_buffer
      - .actual_access:  read_only
        .address_space:  global
        .offset:         48
        .size:           8
        .value_kind:     global_buffer
      - .actual_access:  read_only
        .address_space:  global
        .offset:         56
        .size:           8
        .value_kind:     global_buffer
      - .actual_access:  read_only
        .address_space:  global
        .offset:         64
        .size:           8
        .value_kind:     global_buffer
      - .actual_access:  read_only
        .address_space:  global
        .offset:         72
        .size:           8
        .value_kind:     global_buffer
      - .actual_access:  read_only
        .address_space:  global
        .offset:         80
        .size:           8
        .value_kind:     global_buffer
      - .actual_access:  read_only
        .address_space:  global
        .offset:         88
        .size:           8
        .value_kind:     global_buffer
      - .actual_access:  read_only
        .address_space:  global
        .offset:         96
        .size:           8
        .value_kind:     global_buffer
      - .actual_access:  read_only
        .address_space:  global
        .offset:         104
        .size:           8
        .value_kind:     global_buffer
      - .actual_access:  read_only
        .address_space:  global
        .offset:         112
        .size:           8
        .value_kind:     global_buffer
      - .actual_access:  read_only
        .address_space:  global
        .offset:         120
        .size:           8
        .value_kind:     global_buffer
      - .address_space:  global
        .offset:         128
        .size:           8
        .value_kind:     global_buffer
      - .actual_access:  write_only
        .address_space:  global
        .offset:         136
        .size:           8
        .value_kind:     global_buffer
      - .actual_access:  write_only
        .address_space:  global
        .offset:         144
        .size:           8
        .value_kind:     global_buffer
      - .actual_access:  write_only
        .address_space:  global
        .offset:         152
        .size:           8
        .value_kind:     global_buffer
      - .actual_access:  write_only
        .address_space:  global
        .offset:         160
        .size:           8
        .value_kind:     global_buffer
    .group_segment_fixed_size: 0
    .kernarg_segment_align: 8
    .kernarg_segment_size: 168
    .language:       OpenCL C
    .language_version:
      - 2
      - 0
    .max_flat_workgroup_size: 512
    .name:           _Z10k2_featurePKfPKDF16_S0_S0_S0_S0_S0_S0_PKyS0_S0_S0_S0_S0_S0_S0_PfS5_S5_S5_S5_
    .private_segment_fixed_size: 0
    .sgpr_count:     38
    .sgpr_spill_count: 0
    .symbol:         _Z10k2_featurePKfPKDF16_S0_S0_S0_S0_S0_S0_PKyS0_S0_S0_S0_S0_S0_S0_PfS5_S5_S5_S5_.kd
    .uniform_work_group_size: 1
    .uses_dynamic_stack: false
    .vgpr_count:     256
    .vgpr_spill_count: 0
    .wavefront_size: 64
  - .agpr_count:     0
    .args:
      - .actual_access:  read_only
        .address_space:  global
        .offset:         0
        .size:           8
        .value_kind:     global_buffer
      - .actual_access:  read_only
        .address_space:  global
        .offset:         8
        .size:           8
        .value_kind:     global_buffer
      - .actual_access:  read_only
        .address_space:  global
        .offset:         16
        .size:           8
        .value_kind:     global_buffer
      - .actual_access:  read_only
        .address_space:  global
        .offset:         24
        .size:           8
        .value_kind:     global_buffer
      - .actual_access:  read_only
        .address_space:  global
        .offset:         32
        .size:           8
        .value_kind:     global_buffer
      - .actual_access:  write_only
        .address_space:  global
        .offset:         40
        .size:           8
        .value_kind:     global_buffer
      - .actual_access:  write_only
        .address_space:  global
        .offset:         48
        .size:           8
        .value_kind:     global_buffer
      - .address_space:  global
        .offset:         56
        .size:           8
        .value_kind:     global_buffer
      - .actual_access:  write_only
        .address_space:  global
        .offset:         64
        .size:           8
        .value_kind:     global_buffer
    .group_segment_fixed_size: 56768
    .kernarg_segment_align: 8
    .kernarg_segment_size: 72
    .language:       OpenCL C
    .language_version:
      - 2
      - 0
    .max_flat_workgroup_size: 768
    .name:           _Z5k3_vqPKDF16_S0_S0_S0_PKfPiPfS3_S4_
    .private_segment_fixed_size: 0
    .sgpr_count:     54
    .sgpr_spill_count: 0
    .symbol:         _Z5k3_vqPKDF16_S0_S0_S0_PKfPiPfS3_S4_.kd
    .uniform_work_group_size: 1
    .uses_dynamic_stack: false
    .vgpr_count:     72
    .vgpr_spill_count: 0
    .wavefront_size: 64
  - .agpr_count:     0
    .args:
      - .actual_access:  read_only
        .address_space:  global
        .offset:         0
        .size:           8
        .value_kind:     global_buffer
      - .actual_access:  read_only
        .address_space:  global
        .offset:         8
        .size:           8
        .value_kind:     global_buffer
      - .address_space:  global
        .offset:         16
        .size:           8
        .value_kind:     global_buffer
      - .actual_access:  read_only
        .address_space:  global
        .offset:         24
        .size:           8
        .value_kind:     global_buffer
      - .actual_access:  read_only
        .address_space:  global
        .offset:         32
        .size:           8
        .value_kind:     global_buffer
      - .actual_access:  read_only
        .address_space:  global
        .offset:         40
        .size:           8
        .value_kind:     global_buffer
      - .actual_access:  read_only
        .address_space:  global
        .offset:         48
        .size:           8
        .value_kind:     global_buffer
      - .actual_access:  read_only
        .address_space:  global
        .offset:         56
        .size:           8
        .value_kind:     global_buffer
      - .actual_access:  read_only
        .address_space:  global
        .offset:         64
        .size:           8
        .value_kind:     global_buffer
      - .actual_access:  read_only
        .address_space:  global
        .offset:         72
        .size:           8
        .value_kind:     global_buffer
      - .actual_access:  read_only
        .address_space:  global
        .offset:         80
        .size:           8
        .value_kind:     global_buffer
      - .address_space:  global
        .offset:         88
        .size:           8
        .value_kind:     global_buffer
      - .actual_access:  read_only
        .address_space:  global
        .offset:         96
        .size:           8
        .value_kind:     global_buffer
      - .actual_access:  read_only
        .address_space:  global
        .offset:         104
        .size:           8
        .value_kind:     global_buffer
      - .actual_access:  read_only
        .address_space:  global
        .offset:         112
        .size:           8
        .value_kind:     global_buffer
      - .actual_access:  read_only
        .address_space:  global
        .offset:         120
        .size:           8
        .value_kind:     global_buffer
      - .actual_access:  read_only
        .address_space:  global
        .offset:         128
        .size:           8
        .value_kind:     global_buffer
      - .address_space:  global
        .offset:         136
        .size:           8
        .value_kind:     global_buffer
      - .address_space:  global
        .offset:         144
        .size:           8
        .value_kind:     global_buffer
      - .actual_access:  write_only
        .address_space:  global
        .offset:         152
        .size:           8
        .value_kind:     global_buffer
      - .offset:         160
        .size:           4
        .value_kind:     hidden_block_count_x
      - .offset:         164
        .size:           4
        .value_kind:     hidden_block_count_y
      - .offset:         168
        .size:           4
        .value_kind:     hidden_block_count_z
      - .offset:         172
        .size:           2
        .value_kind:     hidden_group_size_x
      - .offset:         174
        .size:           2
        .value_kind:     hidden_group_size_y
      - .offset:         176
        .size:           2
        .value_kind:     hidden_group_size_z
      - .offset:         178
        .size:           2
        .value_kind:     hidden_remainder_x
      - .offset:         180
        .size:           2
        .value_kind:     hidden_remainder_y
      - .offset:         182
        .size:           2
        .value_kind:     hidden_remainder_z
      - .offset:         200
        .size:           8
        .value_kind:     hidden_global_offset_x
      - .offset:         208
        .size:           8
        .value_kind:     hidden_global_offset_y
      - .offset:         216
        .size:           8
        .value_kind:     hidden_global_offset_z
      - .offset:         224
        .size:           2
        .value_kind:     hidden_grid_dims
      - .offset:         280
        .size:           4
        .value_kind:     hidden_dynamic_lds_size
    .group_segment_fixed_size: 0
    .kernarg_segment_align: 8
    .kernarg_segment_size: 416
    .language:       OpenCL C
    .language_version:
      - 2
      - 0
    .max_flat_workgroup_size: 768
    .name:           _Z7k5_convPKDF16_PKiS0_PKfS4_S4_S4_S4_S4_S4_S4_PfS4_S4_S2_S2_S4_PiS5_S5_
    .private_segment_fixed_size: 0
    .sgpr_count:     51
    .sgpr_spill_count: 0
    .symbol:         _Z7k5_convPKDF16_PKiS0_PKfS4_S4_S4_S4_S4_S4_S4_PfS4_S4_S2_S2_S4_PiS5_S5_.kd
    .uniform_work_group_size: 1
    .uses_dynamic_stack: false
    .vgpr_count:     80
    .vgpr_spill_count: 0
    .wavefront_size: 64
